# MoE weight conversion of layers 1-3 moved from the prologue into the attention phase work queue (interleaved 1:2 with attention items)
# speedup vs baseline: 1.0351x; 1.0236x over previous
.LBB0_20:
	s_mov_b32 s2, 0x83fef803
	v_mul_hi_i32 v2, v1, s2
	v_add_u32_e32 v2, v2, v1
	v_lshrrev_b32_e32 v8, 31, v2
	v_ashrrev_i32_e32 v2, 13, v2
	v_add_u32_e32 v8, v2, v8
	v_mul_i32_i24_e32 v12, 0x3e10, v8
	v_sub_u32_e32 v2, v1, v12
	s_movk_i32 s2, 0xa8f
	v_cmp_lt_i32_e32 vcc, s2, v2
	s_and_saveexec_b64 s[2:3], vcc
	s_xor_b64 s[24:25], exec, s[2:3]
	s_cbranch_execz .LBB0_35
	s_movk_i32 s2, 0xc0f
	v_cmp_lt_u32_e32 vcc, s2, v2
	s_and_saveexec_b64 s[2:3], vcc
	s_xor_b64 s[26:27], exec, s[2:3]
	s_cbranch_execz .LBB0_32
	s_movk_i32 s2, 0xe0f
	v_cmp_lt_u32_e32 vcc, s2, v2
	s_and_saveexec_b64 s[2:3], vcc
	s_xor_b64 s[28:29], exec, s[2:3]
	s_cbranch_execz .LBB0_29
	s_movk_i32 s2, 0x3e10
	v_cmp_gt_i32_e32 vcc, s2, v1
	s_movk_i32 s2, 0x3e0f
	v_cmp_lt_u32_e64 s[2:3], s2, v2
	s_or_b64 s[30:31], vcc, s[2:3]
	s_and_saveexec_b64 s[2:3], s[30:31]
	s_cbranch_execz .LBB0_28
	v_add_u32_e32 v11, 0xfffff1f0, v2
	s_movk_i32 s30, 0x1fff
	v_cmp_lt_u32_e32 vcc, s30, v11
	v_lshlrev_b32_e32 v10, 2, v0
	s_and_saveexec_b64 s[30:31], vcc
	s_xor_b64 s[30:31], exec, s[30:31]
	s_cbranch_execz .LBB0_26
	s_load_dwordx2 s[34:35], s[6:7], 0x70
	v_add_u32_e32 v2, 0xffffd1f0, v2
	v_lshrrev_b32_e32 v2, 7, v2
	v_ashrrev_i32_e32 v9, 31, v8
	v_lshlrev_b64 v[12:13], 20, v[2:3]
	v_lshlrev_b64 v[8:9], 25, v[8:9]
	v_lshlrev_b32_e32 v2, 3, v11
	v_lshl_add_u64 v[8:9], v[12:13], 0, v[8:9]
	v_and_b32_e32 v2, 0x380, v2
	v_lshlrev_b32_e32 v11, 6, v11
	s_waitcnt lgkmcnt(0)
	v_lshl_add_u64 v[12:13], v[8:9], 2, s[34:35]
	v_and_b32_e32 v79, 0x3c0, v11
	v_lshlrev_b32_e32 v14, 12, v2
	v_mov_b32_e32 v15, v3
	v_lshl_add_u64 v[12:13], v[12:13], 0, v[14:15]
	v_lshlrev_b32_e32 v14, 2, v79
	v_lshl_add_u64 v[12:13], v[12:13], 0, v[14:15]
	v_mov_b32_e32 v11, v3
	v_lshl_add_u64 v[10:11], v[12:13], 0, v[10:11]
	s_mov_b32 s34, 0x10000
	v_add_co_u32_e32 v12, vcc, s34, v10
	s_mov_b32 s34, 0xe000
	s_nop 0
	v_addc_co_u32_e32 v13, vcc, 0, v11, vcc
	v_add_co_u32_e32 v14, vcc, s34, v10
	s_mov_b32 s34, 0xd000
	s_nop 0
	v_addc_co_u32_e32 v15, vcc, 0, v11, vcc
	global_load_dword v80, v[12:13], off offset:-4096 nt
	global_load_dword v81, v[14:15], off nt
	v_add_co_u32_e32 v14, vcc, s34, v10
	s_mov_b32 s34, 0xc000
	s_nop 0
	v_addc_co_u32_e32 v15, vcc, 0, v11, vcc
	global_load_dword v82, v[14:15], off nt
	v_add_co_u32_e32 v14, vcc, s34, v10
	s_mov_b32 s34, 0xb000
	s_nop 0
	v_addc_co_u32_e32 v15, vcc, 0, v11, vcc
	global_load_dword v83, v[14:15], off nt
	v_add_co_u32_e32 v14, vcc, s34, v10
	s_mov_b32 s34, 0xa000
	s_nop 0
	v_addc_co_u32_e32 v15, vcc, 0, v11, vcc
	global_load_dword v84, v[14:15], off nt
	v_add_co_u32_e32 v14, vcc, s34, v10
	s_mov_b32 s34, 0x9000
	s_nop 0
	v_addc_co_u32_e32 v15, vcc, 0, v11, vcc
	global_load_dword v85, v[14:15], off nt
	v_add_co_u32_e32 v14, vcc, s34, v10
	s_mov_b32 s34, 0x8000
	s_nop 0
	v_addc_co_u32_e32 v15, vcc, 0, v11, vcc
	global_load_dword v87, v[14:15], off nt
	v_add_co_u32_e32 v14, vcc, s34, v10
	s_movk_i32 s34, 0x7000
	s_nop 0
	v_addc_co_u32_e32 v15, vcc, 0, v11, vcc
	global_load_dword v88, v[14:15], off nt
	v_add_co_u32_e32 v14, vcc, s34, v10
	s_movk_i32 s34, 0x6000
	s_nop 0
	v_addc_co_u32_e32 v15, vcc, 0, v11, vcc
	global_load_dword v92, v[14:15], off nt
	v_add_co_u32_e32 v14, vcc, s34, v10
	s_movk_i32 s34, 0x5000
	s_nop 0
	v_addc_co_u32_e32 v15, vcc, 0, v11, vcc
	global_load_dword v97, v[14:15], off nt
	v_add_co_u32_e32 v14, vcc, s34, v10
	s_movk_i32 s34, 0x4000
	s_nop 0
	v_addc_co_u32_e32 v15, vcc, 0, v11, vcc
	global_load_dword v100, v[14:15], off nt
	v_add_co_u32_e32 v14, vcc, s34, v10
	s_movk_i32 s34, 0x3000
	s_nop 0
	v_addc_co_u32_e32 v15, vcc, 0, v11, vcc
	global_load_dword v105, v[14:15], off nt
	v_add_co_u32_e32 v14, vcc, s34, v10
	s_movk_i32 s34, 0x2000
	s_nop 0
	v_addc_co_u32_e32 v15, vcc, 0, v11, vcc
	global_load_dword v112, v[14:15], off nt
	v_add_co_u32_e32 v14, vcc, s34, v10
	s_movk_i32 s34, 0x1000
	s_nop 0
	v_addc_co_u32_e32 v15, vcc, 0, v11, vcc
	global_load_dword v114, v[14:15], off nt
	v_add_co_u32_e32 v14, vcc, s34, v10
	s_mov_b32 s34, 0x20000
	s_nop 0
	v_addc_co_u32_e32 v15, vcc, 0, v11, vcc
	v_add_co_u32_e32 v122, vcc, s34, v10
	s_mov_b32 s34, 0x1e000
	s_nop 0
	v_addc_co_u32_e32 v123, vcc, 0, v11, vcc
	global_load_dword v120, v[14:15], off nt
	global_load_dword v124, v[10:11], off nt
	v_add_co_u32_e32 v14, vcc, s34, v10
	s_mov_b32 s34, 0x1d000
	s_nop 0
	v_addc_co_u32_e32 v15, vcc, 0, v11, vcc
	global_load_dword v86, v[122:123], off offset:-4096 nt
	global_load_dword v89, v[14:15], off nt
	v_add_co_u32_e32 v14, vcc, s34, v10
	s_mov_b32 s34, 0x1c000
	s_nop 0
	v_addc_co_u32_e32 v15, vcc, 0, v11, vcc
	global_load_dword v90, v[14:15], off nt
	v_add_co_u32_e32 v14, vcc, s34, v10
	s_mov_b32 s34, 0x1b000
	s_nop 0
	v_addc_co_u32_e32 v15, vcc, 0, v11, vcc
	global_load_dword v91, v[14:15], off nt
	v_add_co_u32_e32 v14, vcc, s34, v10
	s_mov_b32 s34, 0x1a000
	s_nop 0
	v_addc_co_u32_e32 v15, vcc, 0, v11, vcc
	global_load_dword v95, v[14:15], off nt
	v_add_co_u32_e32 v14, vcc, s34, v10
	s_mov_b32 s34, 0x19000
	s_nop 0
	v_addc_co_u32_e32 v15, vcc, 0, v11, vcc
	global_load_dword v99, v[14:15], off nt
	v_add_co_u32_e32 v14, vcc, s34, v10
	s_mov_b32 s34, 0x18000
	s_nop 0
	v_addc_co_u32_e32 v15, vcc, 0, v11, vcc
	global_load_dword v104, v[14:15], off nt
	v_add_co_u32_e32 v14, vcc, s34, v10
	s_mov_b32 s34, 0x17000
	s_nop 0
	v_addc_co_u32_e32 v15, vcc, 0, v11, vcc
	global_load_dword v110, v[14:15], off nt
	v_add_co_u32_e32 v14, vcc, s34, v10
	s_mov_b32 s34, 0x16000
	s_nop 0
	v_addc_co_u32_e32 v15, vcc, 0, v11, vcc
	global_load_dword v121, v[14:15], off nt
	v_add_co_u32_e32 v14, vcc, s34, v10
	s_mov_b32 s34, 0x15000
	s_nop 0
	v_addc_co_u32_e32 v15, vcc, 0, v11, vcc
	global_load_dword v126, v[14:15], off nt
	v_add_co_u32_e32 v14, vcc, s34, v10
	s_mov_b32 s34, 0x14000
	s_nop 0
	v_addc_co_u32_e32 v15, vcc, 0, v11, vcc
	global_load_dword v130, v[14:15], off nt
	v_add_co_u32_e32 v14, vcc, s34, v10
	s_mov_b32 s34, 0x13000
	s_nop 0
	v_addc_co_u32_e32 v15, vcc, 0, v11, vcc
	global_load_dword v133, v[14:15], off nt
	v_add_co_u32_e32 v14, vcc, s34, v10
	s_mov_b32 s34, 0x12000
	s_nop 0
	v_addc_co_u32_e32 v15, vcc, 0, v11, vcc
	global_load_dword v137, v[14:15], off nt
	v_add_co_u32_e32 v14, vcc, s34, v10
	s_mov_b32 s34, 0x11000
	s_nop 0
	v_addc_co_u32_e32 v15, vcc, 0, v11, vcc
	global_load_dword v140, v[14:15], off nt
	v_add_co_u32_e32 v14, vcc, s34, v10
	s_mov_b32 s34, 0x2e000
	s_nop 0
	v_addc_co_u32_e32 v15, vcc, 0, v11, vcc
	global_load_dword v141, v[14:15], off nt
	global_load_dword v142, v[12:13], off nt
	v_add_co_u32_e32 v14, vcc, s79, v10
	v_mov_b32_e32 v206, v3
	s_nop 0
	v_addc_co_u32_e32 v15, vcc, 0, v11, vcc
	v_add_co_u32_e32 v12, vcc, s34, v10
	s_mov_b32 s34, 0x2d000
	s_nop 0
	v_addc_co_u32_e32 v13, vcc, 0, v11, vcc
	global_load_dword v102, v[14:15], off offset:-4096 nt
	global_load_dword v106, v[12:13], off nt
	v_add_co_u32_e32 v12, vcc, s34, v10
	s_mov_b32 s34, 0x2c000
	s_nop 0
	v_addc_co_u32_e32 v13, vcc, 0, v11, vcc
	global_load_dword v109, v[12:13], off nt
	v_add_co_u32_e32 v12, vcc, s34, v10
	s_mov_b32 s34, 0x2b000
	s_nop 0
	v_addc_co_u32_e32 v13, vcc, 0, v11, vcc
	global_load_dword v111, v[12:13], off nt
	v_add_co_u32_e32 v12, vcc, s34, v10
	s_mov_b32 s34, 0x2a000
	s_nop 0
	v_addc_co_u32_e32 v13, vcc, 0, v11, vcc
	global_load_dword v113, v[12:13], off nt
	v_add_co_u32_e32 v12, vcc, s34, v10
	s_mov_b32 s34, 0x29000
	s_nop 0
	v_addc_co_u32_e32 v13, vcc, 0, v11, vcc
	global_load_dword v115, v[12:13], off nt
	v_add_co_u32_e32 v12, vcc, s34, v10
	s_mov_b32 s34, 0x28000
	s_nop 0
	v_addc_co_u32_e32 v13, vcc, 0, v11, vcc
	global_load_dword v116, v[12:13], off nt
	v_add_co_u32_e32 v12, vcc, s34, v10
	s_mov_b32 s34, 0x27000
	s_nop 0
	v_addc_co_u32_e32 v13, vcc, 0, v11, vcc
	global_load_dword v119, v[12:13], off nt
	v_add_co_u32_e32 v12, vcc, s34, v10
	s_mov_b32 s34, 0x26000
	s_nop 0
	v_addc_co_u32_e32 v13, vcc, 0, v11, vcc
	global_load_dword v128, v[12:13], off nt
	v_add_co_u32_e32 v12, vcc, s34, v10
	s_mov_b32 s34, 0x25000
	s_nop 0
	v_addc_co_u32_e32 v13, vcc, 0, v11, vcc
	global_load_dword v131, v[12:13], off nt
	v_add_co_u32_e32 v12, vcc, s34, v10
	s_mov_b32 s34, 0x24000
	s_nop 0
	v_addc_co_u32_e32 v13, vcc, 0, v11, vcc
	global_load_dword v132, v[12:13], off nt
	v_add_co_u32_e32 v12, vcc, s34, v10
	s_mov_b32 s34, 0x23000
	s_nop 0
	v_addc_co_u32_e32 v13, vcc, 0, v11, vcc
	global_load_dword v134, v[12:13], off nt
	v_add_co_u32_e32 v12, vcc, s34, v10
	s_mov_b32 s34, 0x21000
	s_nop 0
	v_addc_co_u32_e32 v13, vcc, 0, v11, vcc
	global_load_dword v135, v[12:13], off nt
	v_add_co_u32_e32 v12, vcc, s71, v10
	v_mov_b32_e32 v207, v3
	s_nop 0
	v_addc_co_u32_e32 v13, vcc, 0, v11, vcc
	global_load_dword v136, v[12:13], off nt
	v_add_co_u32_e32 v12, vcc, s34, v10
	s_mov_b32 s34, 0x3d000
	s_nop 0
	v_addc_co_u32_e32 v13, vcc, 0, v11, vcc
	global_load_dword v138, v[12:13], off nt
	global_load_dword v139, v[122:123], off nt
	v_add_co_u32_e32 v12, vcc, s87, v10
	v_lshl_add_u64 v[8:9], s[10:11], 0, v[8:9]
	s_nop 0
	v_addc_co_u32_e32 v13, vcc, 0, v11, vcc
	v_add_co_u32_e32 v122, vcc, s72, v10
	global_load_dword v93, v[12:13], off offset:-4096 nt
	s_nop 0
	v_addc_co_u32_e32 v123, vcc, 0, v11, vcc
	global_load_dword v94, v[122:123], off nt
	v_add_co_u32_e32 v122, vcc, s34, v10
	s_mov_b32 s34, 0x3b000
	s_nop 0
	v_addc_co_u32_e32 v123, vcc, 0, v11, vcc
	global_load_dword v96, v[122:123], off nt
	v_add_co_u32_e32 v122, vcc, s73, v10
	v_lshl_add_u64 v[8:9], v[8:9], 0, v[2:3]
	s_nop 0
	v_addc_co_u32_e32 v123, vcc, 0, v11, vcc
	global_load_dword v98, v[122:123], off nt
	v_add_co_u32_e32 v122, vcc, s34, v10
	s_mov_b32 s34, 0x39000
	s_nop 0
	v_addc_co_u32_e32 v123, vcc, 0, v11, vcc
	global_load_dword v101, v[122:123], off nt
	v_add_co_u32_e32 v122, vcc, s74, v10
	v_or_b32_e32 v2, v79, v18
	s_nop 0
	v_addc_co_u32_e32 v123, vcc, 0, v11, vcc
	global_load_dword v103, v[122:123], off nt
	v_add_co_u32_e32 v122, vcc, s34, v10
	s_mov_b32 s34, 0x37000
	s_nop 0
	v_addc_co_u32_e32 v123, vcc, 0, v11, vcc
	global_load_dword v107, v[122:123], off nt
	v_add_co_u32_e32 v122, vcc, s75, v10
	v_lshlrev_b32_e32 v2, 10, v2
	s_nop 0
	v_addc_co_u32_e32 v123, vcc, 0, v11, vcc
	global_load_dword v108, v[122:123], off nt
	v_add_co_u32_e32 v122, vcc, s34, v10
	s_mov_b32 s34, 0x35000
	s_nop 0
	v_addc_co_u32_e32 v123, vcc, 0, v11, vcc
	global_load_dword v117, v[122:123], off nt
	v_add_co_u32_e32 v122, vcc, s76, v10
	s_nop 1
	v_addc_co_u32_e32 v123, vcc, 0, v11, vcc
	global_load_dword v118, v[122:123], off nt
	v_add_co_u32_e32 v122, vcc, s34, v10
	s_mov_b32 s34, 0x33000
	s_nop 0
	v_addc_co_u32_e32 v123, vcc, 0, v11, vcc
	v_add_co_u32_e32 v144, vcc, s77, v10
	global_load_dword v122, v[122:123], off nt
	s_nop 0
	v_addc_co_u32_e32 v145, vcc, 0, v11, vcc
	global_load_dword v123, v[144:145], off nt
	v_add_co_u32_e32 v144, vcc, s34, v10
	s_mov_b32 s34, 0x31000
	s_nop 0
	v_addc_co_u32_e32 v145, vcc, 0, v11, vcc
	global_load_dword v125, v[144:145], off nt
	v_add_co_u32_e32 v144, vcc, s78, v10
	s_nop 1
	v_addc_co_u32_e32 v145, vcc, 0, v11, vcc
	global_load_dword v127, v[144:145], off nt
	v_add_co_u32_e32 v144, vcc, s34, v10
	s_mov_b32 s34, 0x4d000
	s_nop 0
	v_addc_co_u32_e32 v145, vcc, 0, v11, vcc
	v_add_co_u32_e32 v176, vcc, s95, v10
	global_load_dword v129, v[144:145], off nt
	s_nop 0
	global_load_dword v145, v[14:15], off nt
	v_addc_co_u32_e32 v177, vcc, 0, v11, vcc
	v_add_co_u32_e32 v146, vcc, s80, v10
	global_load_dword v14, v[176:177], off offset:-4096 nt
	s_nop 0
	v_addc_co_u32_e32 v147, vcc, 0, v11, vcc
	global_load_dword v15, v[146:147], off nt
	v_add_co_u32_e32 v146, vcc, s34, v10
	s_mov_b32 s34, 0x4b000
	s_nop 0
	v_addc_co_u32_e32 v147, vcc, 0, v11, vcc
	global_load_dword v143, v[146:147], off nt
	v_add_co_u32_e32 v146, vcc, s81, v10
	s_nop 1
	v_addc_co_u32_e32 v147, vcc, 0, v11, vcc
	global_load_dword v144, v[146:147], off nt
	v_add_co_u32_e32 v146, vcc, s34, v10
	s_mov_b32 s34, 0x49000
	s_nop 0
	v_addc_co_u32_e32 v147, vcc, 0, v11, vcc
	v_add_co_u32_e32 v148, vcc, s82, v10
	global_load_dword v146, v[146:147], off nt
	s_nop 0
	v_addc_co_u32_e32 v149, vcc, 0, v11, vcc
	global_load_dword v147, v[148:149], off nt
	v_add_co_u32_e32 v148, vcc, s34, v10
	s_mov_b32 s34, 0x47000
	s_nop 0
	v_addc_co_u32_e32 v149, vcc, 0, v11, vcc
	global_load_dword v150, v[148:149], off nt
	v_add_co_u32_e32 v148, vcc, s83, v10
	s_nop 1
	v_addc_co_u32_e32 v149, vcc, 0, v11, vcc
	global_load_dword v153, v[148:149], off nt
	v_add_co_u32_e32 v148, vcc, s34, v10
	s_mov_b32 s34, 0x45000
	s_nop 0
	v_addc_co_u32_e32 v149, vcc, 0, v11, vcc
	global_load_dword v158, v[148:149], off nt
	v_add_co_u32_e32 v148, vcc, s84, v10
	s_nop 1
	v_addc_co_u32_e32 v149, vcc, 0, v11, vcc
	global_load_dword v161, v[148:149], off nt
	v_add_co_u32_e32 v148, vcc, s34, v10
	s_mov_b32 s34, 0x43000
	s_nop 0
	v_addc_co_u32_e32 v149, vcc, 0, v11, vcc
	global_load_dword v167, v[148:149], off nt
	v_add_co_u32_e32 v148, vcc, s85, v10
	s_nop 1
	v_addc_co_u32_e32 v149, vcc, 0, v11, vcc
	global_load_dword v170, v[148:149], off nt
	v_add_co_u32_e32 v148, vcc, s34, v10
	s_mov_b32 s34, 0x41000
	s_nop 0
	v_addc_co_u32_e32 v149, vcc, 0, v11, vcc
	global_load_dword v181, v[148:149], off nt
	v_add_co_u32_e32 v148, vcc, s86, v10
	s_nop 1
	v_addc_co_u32_e32 v149, vcc, 0, v11, vcc
	global_load_dword v183, v[148:149], off nt
	v_add_co_u32_e32 v148, vcc, s34, v10
	s_mov_b32 s34, 0x5d000
	s_nop 0
	v_addc_co_u32_e32 v149, vcc, 0, v11, vcc
	v_add_co_u32_e32 v192, vcc, s54, v10
	global_load_dword v186, v[148:149], off nt
	global_load_dword v188, v[12:13], off nt
	v_addc_co_u32_e32 v193, vcc, 0, v11, vcc
	v_add_co_u32_e32 v12, vcc, s88, v10
	global_load_dword v148, v[192:193], off offset:-4096 nt
	s_nop 0
	v_addc_co_u32_e32 v13, vcc, 0, v11, vcc
	global_load_dword v149, v[12:13], off nt
	v_add_co_u32_e32 v12, vcc, s34, v10
	s_mov_b32 s34, 0x5b000
	s_nop 0
	v_addc_co_u32_e32 v13, vcc, 0, v11, vcc
	global_load_dword v151, v[12:13], off nt
	v_add_co_u32_e32 v12, vcc, s89, v10
	s_nop 1
	v_addc_co_u32_e32 v13, vcc, 0, v11, vcc
	global_load_dword v152, v[12:13], off nt
	v_add_co_u32_e32 v12, vcc, s34, v10
	s_mov_b32 s34, 0x59000
	s_nop 0
	v_addc_co_u32_e32 v13, vcc, 0, v11, vcc
	global_load_dword v154, v[12:13], off nt
	v_add_co_u32_e32 v12, vcc, s90, v10
	s_nop 1
	v_addc_co_u32_e32 v13, vcc, 0, v11, vcc
	global_load_dword v155, v[12:13], off nt
	v_add_co_u32_e32 v12, vcc, s34, v10
	s_mov_b32 s34, 0x57000
	s_nop 0
	v_addc_co_u32_e32 v13, vcc, 0, v11, vcc
	global_load_dword v156, v[12:13], off nt
	v_add_co_u32_e32 v12, vcc, s91, v10
	s_nop 1
	v_addc_co_u32_e32 v13, vcc, 0, v11, vcc
	global_load_dword v157, v[12:13], off nt
	v_add_co_u32_e32 v12, vcc, s34, v10
	s_mov_b32 s34, 0x55000
	s_nop 0
	v_addc_co_u32_e32 v13, vcc, 0, v11, vcc
	global_load_dword v162, v[12:13], off nt
	v_add_co_u32_e32 v12, vcc, s92, v10
	s_nop 1
	v_addc_co_u32_e32 v13, vcc, 0, v11, vcc
	global_load_dword v164, v[12:13], off nt
	v_add_co_u32_e32 v12, vcc, s34, v10
	s_mov_b32 s34, 0x53000
	s_nop 0
	v_addc_co_u32_e32 v13, vcc, 0, v11, vcc
	global_load_dword v166, v[12:13], off nt
	v_add_co_u32_e32 v12, vcc, s93, v10
	s_nop 1
	v_addc_co_u32_e32 v13, vcc, 0, v11, vcc
	global_load_dword v168, v[12:13], off nt
	v_add_co_u32_e32 v12, vcc, s34, v10
	s_mov_b32 s34, 0x51000
	s_nop 0
	v_addc_co_u32_e32 v13, vcc, 0, v11, vcc
	global_load_dword v172, v[12:13], off nt
	v_add_co_u32_e32 v12, vcc, s94, v10
	s_nop 1
	v_addc_co_u32_e32 v13, vcc, 0, v11, vcc
	global_load_dword v175, v[12:13], off nt
	v_add_co_u32_e32 v12, vcc, s34, v10
	s_mov_b32 s34, 0x6d000
	s_nop 0
	v_addc_co_u32_e32 v13, vcc, 0, v11, vcc
	global_load_dword v178, v[12:13], off nt
	global_load_dword v179, v[176:177], off nt
	v_add_co_u32_e32 v12, vcc, s62, v10
	s_nop 1
	v_addc_co_u32_e32 v13, vcc, 0, v11, vcc
	v_add_co_u32_e32 v176, vcc, s97, v10
	global_load_dword v173, v[12:13], off offset:-4096 nt
	s_nop 0
	v_addc_co_u32_e32 v177, vcc, 0, v11, vcc
	v_add_co_u32_e32 v184, vcc, s34, v10
	global_load_dword v176, v[176:177], off nt
	s_nop 0
	v_addc_co_u32_e32 v185, vcc, 0, v11, vcc
	global_load_dword v180, v[184:185], off nt
	v_add_co_u32_e32 v184, vcc, s69, v10
	s_mov_b32 s34, 0x6b000
	s_nop 0
	v_addc_co_u32_e32 v185, vcc, 0, v11, vcc
	global_load_dword v182, v[184:185], off nt
	v_add_co_u32_e32 v184, vcc, s34, v10
	s_mov_b32 s34, 0x69000
	s_nop 0
	v_addc_co_u32_e32 v185, vcc, 0, v11, vcc
	v_add_co_u32_e32 v190, vcc, s49, v10
	global_load_dword v184, v[184:185], off nt
	s_nop 0
	v_addc_co_u32_e32 v191, vcc, 0, v11, vcc
	global_load_dword v185, v[190:191], off nt
	v_add_co_u32_e32 v190, vcc, s34, v10
	s_mov_b32 s34, 0x67000
	s_nop 0
	v_addc_co_u32_e32 v191, vcc, 0, v11, vcc
	global_load_dword v189, v[190:191], off nt
	v_add_co_u32_e32 v190, vcc, s50, v10
	s_nop 1
	v_addc_co_u32_e32 v191, vcc, 0, v11, vcc
	v_add_co_u32_e32 v194, vcc, s34, v10
	global_load_dword v191, v[190:191], off nt
	s_nop 0
	v_addc_co_u32_e32 v195, vcc, 0, v11, vcc
	global_load_dword v196, v[194:195], off nt
	v_add_co_u32_e32 v194, vcc, s51, v10
	s_mov_b32 s34, 0x65000
	s_nop 0
	v_addc_co_u32_e32 v195, vcc, 0, v11, vcc
	global_load_dword v197, v[194:195], off nt
	v_add_co_u32_e32 v194, vcc, s34, v10
	s_mov_b32 s34, 0x63000
	s_nop 0
	v_addc_co_u32_e32 v195, vcc, 0, v11, vcc
	global_load_dword v198, v[194:195], off nt
	v_add_co_u32_e32 v194, vcc, s52, v10
	s_nop 1
	v_addc_co_u32_e32 v195, vcc, 0, v11, vcc
	global_load_dword v199, v[194:195], off nt
	v_add_co_u32_e32 v194, vcc, s34, v10
	s_mov_b32 s34, 0x61000
	s_nop 0
	v_addc_co_u32_e32 v195, vcc, 0, v11, vcc
	global_load_dword v200, v[194:195], off nt
	v_add_co_u32_e32 v194, vcc, s53, v10
	s_nop 1
	v_addc_co_u32_e32 v195, vcc, 0, v11, vcc
	global_load_dword v201, v[194:195], off nt
	v_add_co_u32_e32 v194, vcc, s34, v10
	s_mov_b32 s34, 0x7f000
	s_nop 0
	v_addc_co_u32_e32 v195, vcc, 0, v11, vcc
	global_load_dword v202, v[194:195], off nt
	global_load_dword v203, v[192:193], off nt
	v_add_co_u32_e32 v192, vcc, s34, v10
	s_mov_b32 s34, 0x7d000
	s_nop 0
	v_addc_co_u32_e32 v193, vcc, 0, v11, vcc
	global_load_dword v159, v[192:193], off nt
	v_add_co_u32_e32 v192, vcc, s55, v10
	s_nop 1
	v_addc_co_u32_e32 v193, vcc, 0, v11, vcc
	global_load_dword v160, v[192:193], off nt
	v_add_co_u32_e32 v192, vcc, s34, v10
	s_mov_b32 s34, 0x7b000
	s_nop 0
	v_addc_co_u32_e32 v193, vcc, 0, v11, vcc
	global_load_dword v163, v[192:193], off nt
	v_add_co_u32_e32 v192, vcc, s56, v10
	s_nop 1
	v_addc_co_u32_e32 v193, vcc, 0, v11, vcc
	global_load_dword v165, v[192:193], off nt
	v_add_co_u32_e32 v192, vcc, s34, v10
	s_mov_b32 s34, 0x79000
	s_nop 0
	v_addc_co_u32_e32 v193, vcc, 0, v11, vcc
	global_load_dword v169, v[192:193], off nt
	v_add_co_u32_e32 v192, vcc, s57, v10
	s_nop 1
	v_addc_co_u32_e32 v193, vcc, 0, v11, vcc
	global_load_dword v171, v[192:193], off nt
	v_add_co_u32_e32 v192, vcc, s34, v10
	s_mov_b32 s34, 0x77000
	s_nop 0
	v_addc_co_u32_e32 v193, vcc, 0, v11, vcc
	global_load_dword v174, v[192:193], off nt
	v_add_co_u32_e32 v192, vcc, s58, v10
	s_nop 1
	v_addc_co_u32_e32 v193, vcc, 0, v11, vcc
	global_load_dword v177, v[192:193], off nt
	v_add_co_u32_e32 v192, vcc, s34, v10
	s_mov_b32 s34, 0x75000
	s_nop 0
	v_addc_co_u32_e32 v193, vcc, 0, v11, vcc
	global_load_dword v187, v[192:193], off nt
	v_add_co_u32_e32 v192, vcc, s59, v10
	s_nop 1
	v_addc_co_u32_e32 v193, vcc, 0, v11, vcc
	global_load_dword v190, v[192:193], off nt
	v_add_co_u32_e32 v192, vcc, s34, v10
	s_mov_b32 s34, 0x73000
	s_nop 0
	v_addc_co_u32_e32 v193, vcc, 0, v11, vcc
	v_add_co_u32_e32 v194, vcc, s60, v10
	global_load_dword v192, v[192:193], off nt
	s_nop 0
	v_addc_co_u32_e32 v195, vcc, 0, v11, vcc
	global_load_dword v193, v[194:195], off nt
	v_add_co_u32_e32 v194, vcc, s34, v10
	s_mov_b32 s34, 0x71000
	s_nop 0
	v_addc_co_u32_e32 v195, vcc, 0, v11, vcc
	v_add_co_u32_e32 v204, vcc, s61, v10
	global_load_dword v194, v[194:195], off nt
	s_nop 0
	v_addc_co_u32_e32 v205, vcc, 0, v11, vcc
	v_add_co_u32_e32 v10, vcc, s34, v10
	global_load_dword v195, v[204:205], off nt
	s_nop 0
	v_addc_co_u32_e32 v11, vcc, 0, v11, vcc
	global_load_dword v10, v[10:11], off nt
	s_nop 0
	global_load_dword v11, v[12:13], off nt
	s_waitcnt vmcnt(62)
	v_mov_b32_e32 v204, v3
	v_mul_f32_e32 v12, 0x42800000, v124
	v_mul_f32_e32 v13, 0x42800000, v120
	v_cvt_pk_fp8_f32 v204, v12, v13
	v_mul_f32_e32 v12, 0x42800000, v105
	v_mul_f32_e32 v13, 0x42800000, v100
	v_mov_b32_e32 v205, v3
	v_cvt_pk_fp8_f32 v205, v12, v13
	v_mul_f32_e32 v12, 0x42800000, v88
	v_mul_f32_e32 v13, 0x42800000, v87
	v_cvt_pk_fp8_f32 v206, v12, v13
	v_mul_f32_e32 v12, 0x42800000, v83
	v_mul_f32_e32 v13, 0x42800000, v82
	v_cvt_pk_fp8_f32 v207, v12, v13
	v_mul_f32_e32 v81, 0x42800000, v81
	v_mul_f32_e32 v80, 0x42800000, v80
	v_cvt_pk_fp8_f32 v207, v81, v80 op_sel:[0,0,1]
	v_mul_f32_e32 v13, 0x42800000, v142
	v_mul_f32_e32 v81, 0x42800000, v141
	v_mov_b32_e32 v80, v3
	v_cvt_pk_fp8_f32 v80, v13, v81
	v_mul_f32_e32 v82, 0x42800000, v140
	v_mul_f32_e32 v83, 0x42800000, v137
	v_mul_f32_e32 v13, 0x42800000, v133
	v_cvt_pk_fp8_f32 v80, v82, v83 op_sel:[0,0,1]
	v_mul_f32_e32 v82, 0x42800000, v130
	v_mov_b32_e32 v81, v3
	v_cvt_pk_fp8_f32 v81, v13, v82
	v_mul_f32_e32 v85, 0x42800000, v85
	v_mul_f32_e32 v84, 0x42800000, v84
	v_cvt_pk_fp8_f32 v206, v85, v84 op_sel:[0,0,1]
	v_mul_f32_e32 v83, 0x42800000, v126
	v_mul_f32_e32 v84, 0x42800000, v121
	v_cvt_pk_fp8_f32 v81, v83, v84 op_sel:[0,0,1]
	v_mul_f32_e32 v13, 0x42800000, v110
	v_mul_f32_e32 v83, 0x42800000, v104
	v_mov_b32_e32 v82, v3
	v_cvt_pk_fp8_f32 v82, v13, v83
	v_mul_f32_e32 v84, 0x42800000, v99
	v_mul_f32_e32 v85, 0x42800000, v95
	v_mul_f32_e32 v13, 0x42800000, v91
	v_cvt_pk_fp8_f32 v82, v84, v85 op_sel:[0,0,1]
	v_mul_f32_e32 v84, 0x42800000, v90
	v_mov_b32_e32 v83, v3
	v_cvt_pk_fp8_f32 v83, v13, v84
	v_mul_f32_e32 v85, 0x42800000, v89
	v_mul_f32_e32 v86, 0x42800000, v86
	v_add_u32_e32 v12, v16, v17
	v_cvt_pk_fp8_f32 v83, v85, v86 op_sel:[0,0,1]
	s_waitcnt vmcnt(48)
	s_waitcnt vmcnt(32)
	s_waitcnt vmcnt(16)
	s_waitcnt vmcnt(0)
	ds_write_b128 v12, v[80:83] offset:16
	v_mul_f32_e32 v13, 0x42800000, v139
	v_mul_f32_e32 v81, 0x42800000, v138
	v_mov_b32_e32 v80, v3
	v_cvt_pk_fp8_f32 v80, v13, v81
	v_mul_f32_e32 v82, 0x42800000, v136
	v_mul_f32_e32 v83, 0x42800000, v135
	v_mul_f32_e32 v13, 0x42800000, v134
	v_cvt_pk_fp8_f32 v80, v82, v83 op_sel:[0,0,1]
	v_mul_f32_e32 v82, 0x42800000, v132
	v_mov_b32_e32 v81, v3
	v_cvt_pk_fp8_f32 v81, v13, v82
	v_mul_f32_e32 v83, 0x42800000, v131
	v_mul_f32_e32 v84, 0x42800000, v128
	v_mul_f32_e32 v13, 0x42800000, v119
	v_cvt_pk_fp8_f32 v81, v83, v84 op_sel:[0,0,1]
	v_mul_f32_e32 v83, 0x42800000, v116
	v_mov_b32_e32 v82, v3
	v_cvt_pk_fp8_f32 v82, v13, v83
	v_mul_f32_e32 v84, 0x42800000, v115
	v_mul_f32_e32 v85, 0x42800000, v113
	v_mul_f32_e32 v13, 0x42800000, v111
	v_cvt_pk_fp8_f32 v82, v84, v85 op_sel:[0,0,1]
	v_mul_f32_e32 v84, 0x42800000, v109
	v_mov_b32_e32 v83, v3
	v_cvt_pk_fp8_f32 v83, v13, v84
	v_mul_f32_e32 v85, 0x42800000, v106
	v_mul_f32_e32 v86, 0x42800000, v102
	v_mul_f32_e32 v13, 0x42800000, v145
	v_cvt_pk_fp8_f32 v83, v85, v86 op_sel:[0,0,1]
	v_mul_f32_e32 v84, 0x42800000, v117
	v_mul_f32_e32 v85, 0x42800000, v101
	v_mul_f32_e32 v86, 0x42800000, v93
	ds_write_b128 v12, v[80:83] offset:32
	v_mul_f32_e32 v81, 0x42800000, v129
	v_mov_b32_e32 v80, v3
	v_cvt_pk_fp8_f32 v80, v13, v81
	v_mul_f32_e32 v82, 0x42800000, v127
	v_mul_f32_e32 v83, 0x42800000, v125
	v_mul_f32_e32 v13, 0x42800000, v123
	v_cvt_pk_fp8_f32 v80, v82, v83 op_sel:[0,0,1]
	v_mul_f32_e32 v82, 0x42800000, v122
	v_mov_b32_e32 v81, v3
	v_cvt_pk_fp8_f32 v81, v13, v82
	v_mul_f32_e32 v83, 0x42800000, v118
	v_mul_f32_e32 v13, 0x42800000, v108
	v_mov_b32_e32 v82, v3
	v_cvt_pk_fp8_f32 v81, v83, v84 op_sel:[0,0,1]
	v_mul_f32_e32 v83, 0x42800000, v107
	v_cvt_pk_fp8_f32 v82, v13, v83
	v_mul_f32_e32 v84, 0x42800000, v103
	v_mul_f32_e32 v13, 0x42800000, v98
	v_mov_b32_e32 v83, v3
	v_cvt_pk_fp8_f32 v82, v84, v85 op_sel:[0,0,1]
	v_mul_f32_e32 v84, 0x42800000, v96
	v_cvt_pk_fp8_f32 v83, v13, v84
	v_mul_f32_e32 v85, 0x42800000, v94
	v_mul_f32_e32 v13, 0x42800000, v188
	v_mul_f32_e32 v84, 0x42800000, v158
	v_cvt_pk_fp8_f32 v83, v85, v86 op_sel:[0,0,1]
	v_mul_f32_e32 v85, 0x42800000, v146
	v_mul_f32_e32 v15, 0x42800000, v15
	v_mul_f32_e32 v14, 0x42800000, v14
	ds_write_b128 v12, v[80:83] offset:48
	v_mul_f32_e32 v81, 0x42800000, v186
	v_mov_b32_e32 v80, v3
	v_cvt_pk_fp8_f32 v80, v13, v81
	v_mul_f32_e32 v82, 0x42800000, v183
	v_mul_f32_e32 v83, 0x42800000, v181
	v_mul_f32_e32 v13, 0x42800000, v170
	v_cvt_pk_fp8_f32 v80, v82, v83 op_sel:[0,0,1]
	v_mul_f32_e32 v82, 0x42800000, v167
	v_mov_b32_e32 v81, v3
	v_cvt_pk_fp8_f32 v81, v13, v82
	v_mul_f32_e32 v83, 0x42800000, v161
	v_mul_f32_e32 v13, 0x42800000, v153
	v_mov_b32_e32 v82, v3
	v_cvt_pk_fp8_f32 v81, v83, v84 op_sel:[0,0,1]
	v_mul_f32_e32 v83, 0x42800000, v150
	v_cvt_pk_fp8_f32 v82, v13, v83
	v_mul_f32_e32 v84, 0x42800000, v147
	v_mul_f32_e32 v13, 0x42800000, v144
	v_mov_b32_e32 v83, v3
	v_cvt_pk_fp8_f32 v82, v84, v85 op_sel:[0,0,1]
	v_mul_f32_e32 v84, 0x42800000, v143
	v_cvt_pk_fp8_f32 v83, v13, v84
	v_mul_f32_e32 v13, 0x42800000, v179
	v_mul_f32_e32 v84, 0x42800000, v148
	v_mul_f32_e32 v11, 0x42800000, v11
	v_cvt_pk_fp8_f32 v83, v15, v14 op_sel:[0,0,1]
	v_mul_f32_e32 v14, 0x42800000, v178
	v_mul_f32_e32 v15, 0x42800000, v175
	v_mul_f32_e32 v10, 0x42800000, v10
	ds_write_b128 v12, v[80:83] offset:64
	v_mov_b32_e32 v80, v3
	v_cvt_pk_fp8_f32 v80, v13, v14
	v_mul_f32_e32 v81, 0x42800000, v172
	v_mul_f32_e32 v13, 0x42800000, v168
	v_mul_f32_e32 v14, 0x42800000, v166
	v_cvt_pk_fp8_f32 v80, v15, v81 op_sel:[0,0,1]
	v_mov_b32_e32 v81, v3
	v_cvt_pk_fp8_f32 v81, v13, v14
	v_mul_f32_e32 v15, 0x42800000, v164
	v_mul_f32_e32 v82, 0x42800000, v162
	v_mul_f32_e32 v13, 0x42800000, v157
	v_cvt_pk_fp8_f32 v81, v15, v82 op_sel:[0,0,1]
	v_mul_f32_e32 v14, 0x42800000, v156
	v_mov_b32_e32 v82, v3
	v_cvt_pk_fp8_f32 v82, v13, v14
	v_mul_f32_e32 v15, 0x42800000, v155
	v_mul_f32_e32 v83, 0x42800000, v154
	v_mul_f32_e32 v13, 0x42800000, v152
	v_cvt_pk_fp8_f32 v82, v15, v83 op_sel:[0,0,1]
	v_mul_f32_e32 v14, 0x42800000, v151
	v_mov_b32_e32 v83, v3
	v_cvt_pk_fp8_f32 v83, v13, v14
	v_mul_f32_e32 v15, 0x42800000, v149
	v_mul_f32_e32 v13, 0x42800000, v203
	v_mul_f32_e32 v14, 0x42800000, v202
	v_cvt_pk_fp8_f32 v83, v15, v84 op_sel:[0,0,1]
	v_mul_f32_e32 v15, 0x42800000, v201
	v_mul_f32_e32 v84, 0x42800000, v173
	v_mul_f32_e32 v114, 0x42800000, v114
	ds_write_b128 v12, v[80:83] offset:80
	v_mov_b32_e32 v80, v3
	v_cvt_pk_fp8_f32 v80, v13, v14
	v_mul_f32_e32 v81, 0x42800000, v200
	v_mul_f32_e32 v13, 0x42800000, v199
	v_mul_f32_e32 v14, 0x42800000, v198
	v_cvt_pk_fp8_f32 v80, v15, v81 op_sel:[0,0,1]
	v_mov_b32_e32 v81, v3
	v_cvt_pk_fp8_f32 v81, v13, v14
	v_mul_f32_e32 v15, 0x42800000, v197
	v_mul_f32_e32 v82, 0x42800000, v196
	v_mul_f32_e32 v13, 0x42800000, v191
	v_cvt_pk_fp8_f32 v81, v15, v82 op_sel:[0,0,1]
	v_mul_f32_e32 v14, 0x42800000, v189
	v_mov_b32_e32 v82, v3
	v_cvt_pk_fp8_f32 v82, v13, v14
	v_mul_f32_e32 v15, 0x42800000, v185
	v_mul_f32_e32 v83, 0x42800000, v184
	v_mul_f32_e32 v13, 0x42800000, v182
	v_cvt_pk_fp8_f32 v82, v15, v83 op_sel:[0,0,1]
	v_mul_f32_e32 v14, 0x42800000, v180
	v_mov_b32_e32 v83, v3
	v_cvt_pk_fp8_f32 v83, v13, v14
	v_mul_f32_e32 v15, 0x42800000, v176
	v_mul_f32_e32 v13, 0x42800000, v195
	v_mul_f32_e32 v14, 0x42800000, v194
	v_cvt_pk_fp8_f32 v83, v15, v84 op_sel:[0,0,1]
	v_mul_f32_e32 v112, 0x42800000, v112
	v_mul_f32_e32 v97, 0x42800000, v97
	v_mul_f32_e32 v92, 0x42800000, v92
	ds_write_b128 v12, v[80:83] offset:96
	v_mov_b32_e32 v80, v3
	v_cvt_pk_fp8_f32 v80, v11, v10
	v_mul_f32_e32 v10, 0x42800000, v193
	v_mul_f32_e32 v11, 0x42800000, v192
	v_mov_b32_e32 v81, v3
	v_cvt_pk_fp8_f32 v81, v10, v11
	v_mul_f32_e32 v10, 0x42800000, v177
	v_mul_f32_e32 v11, 0x42800000, v174
	v_mov_b32_e32 v82, v3
	v_cvt_pk_fp8_f32 v82, v10, v11
	v_mul_f32_e32 v10, 0x42800000, v165
	v_mul_f32_e32 v11, 0x42800000, v163
	v_mov_b32_e32 v83, v3
	v_cvt_pk_fp8_f32 v83, v10, v11
	v_cvt_pk_fp8_f32 v80, v13, v14 op_sel:[0,0,1]
	v_mul_f32_e32 v13, 0x42800000, v190
	v_mul_f32_e32 v14, 0x42800000, v187
	v_cvt_pk_fp8_f32 v81, v13, v14 op_sel:[0,0,1]
	v_mul_f32_e32 v13, 0x42800000, v171
	v_mul_f32_e32 v14, 0x42800000, v169
	v_cvt_pk_fp8_f32 v82, v13, v14 op_sel:[0,0,1]
	v_mul_f32_e32 v13, 0x42800000, v160
	v_mul_f32_e32 v14, 0x42800000, v159
	v_cvt_pk_fp8_f32 v204, v114, v112 op_sel:[0,0,1]
	v_cvt_pk_fp8_f32 v205, v97, v92 op_sel:[0,0,1]
	v_cvt_pk_fp8_f32 v83, v13, v14 op_sel:[0,0,1]
	ds_write_b128 v12, v[204:207]
	ds_write_b128 v12, v[80:83] offset:112
	s_waitcnt lgkmcnt(0)
	v_add_u32_e32 v80, v19, v20
	v_lshl_add_u64 v[12:13], v[8:9], 0, v[4:5]
	ds_read_b128 v[8:11], v80
	v_lshl_add_u64 v[14:15], v[12:13], 0, v[2:3]
	v_or_b32_e32 v2, v79, v21
	v_lshlrev_b32_e32 v2, 10, v2
	s_waitcnt lgkmcnt(0)
	global_store_dwordx4 v[14:15], v[8:11], off
	ds_read_b128 v[8:11], v80 offset:1152
	v_lshl_add_u64 v[14:15], v[12:13], 0, v[2:3]
	v_or_b32_e32 v2, v79, v22
	v_lshlrev_b32_e32 v2, 10, v2
	s_waitcnt lgkmcnt(0)
	global_store_dwordx4 v[14:15], v[8:11], off
	ds_read_b128 v[8:11], v80 offset:2304
	v_lshl_add_u64 v[14:15], v[12:13], 0, v[2:3]
	v_or_b32_e32 v2, v79, v23
	v_lshlrev_b32_e32 v2, 10, v2
	s_waitcnt lgkmcnt(0)
	global_store_dwordx4 v[14:15], v[8:11], off
	ds_read_b128 v[8:11], v80 offset:3456
	v_lshl_add_u64 v[14:15], v[12:13], 0, v[2:3]
	v_or_b32_e32 v2, v79, v24
	v_lshlrev_b32_e32 v2, 10, v2
	s_waitcnt lgkmcnt(0)
	global_store_dwordx4 v[14:15], v[8:11], off
	ds_read_b128 v[8:11], v80 offset:4608
	v_lshl_add_u64 v[14:15], v[12:13], 0, v[2:3]
	v_or_b32_e32 v2, v79, v25
	v_lshlrev_b32_e32 v2, 10, v2
	s_waitcnt lgkmcnt(0)
	global_store_dwordx4 v[14:15], v[8:11], off
	ds_read_b128 v[8:11], v80 offset:5760
	v_lshl_add_u64 v[14:15], v[12:13], 0, v[2:3]
	v_or_b32_e32 v2, v79, v26
	v_lshlrev_b32_e32 v2, 10, v2
	s_waitcnt lgkmcnt(0)
	global_store_dwordx4 v[14:15], v[8:11], off
	ds_read_b128 v[8:11], v80 offset:6912
	v_lshl_add_u64 v[14:15], v[12:13], 0, v[2:3]
	v_or_b32_e32 v2, v79, v27
	v_lshlrev_b32_e32 v2, 10, v2
	v_lshl_add_u64 v[12:13], v[12:13], 0, v[2:3]
	s_waitcnt lgkmcnt(0)
	global_store_dwordx4 v[14:15], v[8:11], off
	ds_read_b128 v[8:11], v80 offset:8064
	s_waitcnt lgkmcnt(0)
	global_store_dwordx4 v[12:13], v[8:11], off
	s_waitcnt lgkmcnt(0)

.LBB0_789:
	s_or_b64 exec, exec, s[2:3]
	v_readlane_b32 s2, v253, 55
	s_waitcnt lgkmcnt(0)
	s_barrier
	v_mov_b32_e32 v0, s2
	v_readlane_b32 s2, v253, 54
	ds_read_b32 v0, v0
	s_nop 0
	v_mov_b32_e32 v1, s2
	ds_read_b32 v1, v1
	s_waitcnt lgkmcnt(0)
	s_barrier
	v_add_u32_e32 v201, 0x580, v0
	s_nop 0
	v_readfirstlane_b32 s100, v201
	v_readlane_b32 s101, v254, 38
	s_nop 3
	s_cmp_eq_u32 s101, 3
	s_cselect_b32 s101, 0, 0x4c0
	s_add_i32 vcc_lo, s100, s101
	s_mul_i32 vcc_hi, s101, 3
	s_max_u32 vcc_lo, vcc_lo, vcc_hi
	v_mov_b32_e32 v201, vcc_lo
	v_readfirstlane_b32 s30, v0
	v_cmp_ge_i32_e32 vcc, v1, v201
	v_readfirstlane_b32 s24, v1
	s_cbranch_vccnz .LBB0_931
	s_add_u32 s31, s4, 0x37b00000
	s_addc_u32 s34, s5, 0
	s_add_i32 s35, s30, 0x480
	s_add_u32 s44, s4, 0x61800000
	s_addc_u32 s45, s5, 0
	s_add_u32 s46, s4, 0x42c00000
	s_addc_u32 s47, s5, 0
	s_add_u32 s10, s4, 0x66d00000
	s_addc_u32 s11, s5, 0
	s_add_u32 s48, s4, 0x61640000
	s_movk_i32 s2, 0x100
	s_addc_u32 s49, s5, 0
	v_cmp_gt_i32_e64 s[38:39], s2, v199
	s_add_i32 s2, 0, 0x14800
	v_add_u32_e32 v214, s2, v200
	s_add_i32 s2, 0, 0x16800
	s_cmp_lg_u32 0, -1
	v_lshlrev_b32_e32 v3, 1, v199
	v_lshlrev_b32_e32 v211, 4, v199
	s_cselect_b32 s3, 0, 0
	v_lshlrev_b32_e32 v0, 3, v199
	v_lshlrev_b32_e32 v1, 10, v101
	v_lshlrev_b32_e32 v2, 4, v198
	v_and_b32_e32 v3, 32, v3
	v_and_b32_e32 v5, 0xc0, v211
	s_addk_i32 s3, 0x6000
	v_and_b32_e32 v210, 24, v0
	v_lshl_or_b32 v5, v101, 8, v5
	v_add3_u32 v213, 0, v1, v2
	v_add_u32_e32 v1, s3, v3
	v_add3_u32 v217, v1, v210, v5
	v_lshrrev_b32_e32 v1, 3, v100
	v_lshl_add_u32 v215, v198, 2, s2
	v_and_b32_e32 v218, 56, v0
	v_lshl_add_u32 v220, v1, 2, s2
	s_add_i32 s2, 0, 0x14a00
	v_add_u32_e32 v4, 0, v3
	v_lshlrev_b32_e32 v96, 1, v218
	v_add_u32_e32 v221, s2, v200
	s_add_i32 s2, 0, 0x14900
	v_ashrrev_i32_e32 v203, 31, v202
	v_lshlrev_b32_e32 v208, 9, v100
	v_lshrrev_b32_e32 v209, 2, v100
	v_add3_u32 v212, v4, v210, v5
	v_cmp_gt_u32_e64 s[40:41], 32, v100
	v_cmp_lt_u32_e64 s[42:43], 31, v100
	v_or_b32_e32 v216, 0xc0, v206
	v_lshl_add_u64 v[204:205], s[4:5], 0, v[96:97]
	v_lshlrev_b32_e32 v219, 7, v1
	v_add_u32_e32 v222, s2, v200
	v_lshlrev_b32_e32 v96, 1, v98
	s_branch .LBB0_792

.LBB0_796:
	s_or_b64 exec, exec, s[2:3]
	v_readlane_b32 s101, v254, 38
	s_nop 3
	s_cmp_eq_u32 s101, 3
	s_cbranch_scc1 .Lc3_attn
	s_cmpk_lt_u32 s24, 0xe40
	s_cbranch_scc0 .Lc3_late
	s_mul_hi_u32 s101, s24, 0xaaaaaaab
	s_lshr_b32 s101, s101, 1
	s_mul_i32 s2, s101, 3
	s_sub_i32 s2, s24, s2
	s_cmp_eq_u32 s2, 2
	s_cbranch_scc1 .Lc3_entry
	s_sub_i32 s24, s24, s101
	s_branch .Lc3_chk
.Lc3_late:
	s_sub_i32 s24, s24, 0x4c0
.Lc3_chk:
	s_cmp_ge_i32 s24, s100
	s_cbranch_scc1 .LBB0_869
.Lc3_attn:
	v_readfirstlane_b32 s2, v199
	s_ashr_i32 s2, s2, 1
	s_andn2_b32 s2, s2, 31
	v_or_b32_e32 v0, s2, v198
	s_mov_b64 s[20:21], 0
	s_cmpk_gt_i32 s24, 0x47f
	v_readfirstlane_b32 s2, v0
	v_readfirstlane_b32 s22, v0
	v_readfirstlane_b32 s23, v1
	s_cbranch_scc0 .LBB0_807
	s_cmp_ge_i32 s24, s35
	s_cselect_b64 s[16:17], -1, 0
	s_add_i32 s3, s24, 0xfffffb80
	s_mov_b64 s[12:13], -1
	s_and_b64 vcc, exec, s[16:17]
	v_readfirstlane_b32 s2, v0
	v_readfirstlane_b32 s22, v0
	s_cbranch_vccnz .LBB0_803
	s_mov_b32 s12, 0
	s_movk_i32 s2, 0xfc

.Lc3_entry:
	v_mov_b32_e32 v139, 0
	v_readlane_b32 s22, v252, 0
	v_readlane_b32 s23, v252, 1
	v_readlane_b32 s20, v254, 38
	s_lshr_b32 s2, s93, 6
	s_load_dwordx2 s[24:25], s[22:23], 0x98
	s_lshl_b32 s3, s2, 14
	s_add_i32 s18, s3, 0
	s_add_i32 s20, s20, 1
	v_mbcnt_lo_u32_b32 v6, -1, 0
	v_mbcnt_hi_u32_b32 v6, -1, v6
	s_lshl_b32 s19, s101, 3
	s_add_i32 s19, s19, s2
	s_addk_i32 s19, 0xa00
	s_waitcnt lgkmcnt(0)
	s_add_u32 s16, s24, 0x3b00000
	s_addc_u32 s17, s25, 0
	s_mov_b64 s[2:3], -1
	s_cmpk_gt_i32 s19, 0x1fff
	v_lshlrev_b32_e32 v138, 2, v6
	s_cbranch_scc0 .Lc3_1477
	s_add_i32 s2, s19, 0xffffe000
	s_lshr_b32 s86, s2, 7
	s_load_dwordx2 s[2:3], s[22:23], 0x70
	s_lshl_b64 s[12:13], s[86:87], 20
	s_lshl_b32 s21, s20, 25
	s_add_u32 s12, s12, s21
	s_addc_u32 s13, s13, 0
	s_lshl_b64 s[14:15], s[12:13], 2
	s_waitcnt lgkmcnt(0)
	s_add_u32 s2, s2, s14
	s_addc_u32 s3, s3, s15
	s_add_u32 s24, s24, s12
	s_addc_u32 s25, s25, s13
	s_lshl_b32 s21, s19, 3
	s_and_b32 s12, s21, 0x380
	s_lshl_b32 s21, s19, 6
	s_and_b32 s21, s21, 0x3c0
	s_lshl_b32 s13, s12, 12
	s_add_u32 s2, s2, s13
	s_addc_u32 s3, s3, 0
	s_lshl_b32 s13, s21, 2
	s_add_u32 s2, s2, s13
	s_addc_u32 s3, s3, 0
	v_lshl_add_u64 v[0:1], s[2:3], 0, v[138:139]
	s_mov_b32 s13, 0x10000
	v_add_co_u32_e32 v2, vcc, s13, v0
	s_mov_b32 s13, 0xe000
	s_nop 0
	v_addc_co_u32_e32 v3, vcc, 0, v1, vcc
	v_add_co_u32_e32 v4, vcc, s13, v0
	s_mov_b32 s13, 0xd000
	s_nop 0
	v_addc_co_u32_e32 v5, vcc, 0, v1, vcc
	global_load_dword v7, v[2:3], off offset:-4096 nt
	global_load_dword v8, v[4:5], off nt
	v_add_co_u32_e32 v4, vcc, s13, v0
	s_mov_b32 s13, 0xc000
	s_nop 0
	v_addc_co_u32_e32 v5, vcc, 0, v1, vcc
	global_load_dword v9, v[4:5], off nt
	v_add_co_u32_e32 v4, vcc, s13, v0
	s_mov_b32 s13, 0xb000
	s_nop 0
	v_addc_co_u32_e32 v5, vcc, 0, v1, vcc
	global_load_dword v10, v[4:5], off nt
	v_add_co_u32_e32 v4, vcc, s13, v0
	s_mov_b32 s13, 0xa000
	s_nop 0
	v_addc_co_u32_e32 v5, vcc, 0, v1, vcc
	global_load_dword v11, v[4:5], off nt
	v_add_co_u32_e32 v4, vcc, s13, v0
	s_mov_b32 s13, 0x9000
	s_nop 0
	v_addc_co_u32_e32 v5, vcc, 0, v1, vcc
	global_load_dword v12, v[4:5], off nt
	v_add_co_u32_e32 v4, vcc, s13, v0
	s_mov_b32 s13, 0x8000
	s_nop 0
	v_addc_co_u32_e32 v5, vcc, 0, v1, vcc
	global_load_dword v13, v[4:5], off nt
	v_add_co_u32_e32 v4, vcc, s13, v0
	s_movk_i32 s13, 0x7000
	s_nop 0
	v_addc_co_u32_e32 v5, vcc, 0, v1, vcc
	global_load_dword v14, v[4:5], off nt
	v_add_co_u32_e32 v4, vcc, s13, v0
	s_movk_i32 s13, 0x6000
	s_nop 0
	v_addc_co_u32_e32 v5, vcc, 0, v1, vcc
	global_load_dword v15, v[4:5], off nt
	v_add_co_u32_e32 v4, vcc, s13, v0
	s_movk_i32 s13, 0x5000
	s_nop 0
	v_addc_co_u32_e32 v5, vcc, 0, v1, vcc
	global_load_dword v16, v[4:5], off nt
	v_add_co_u32_e32 v4, vcc, s13, v0
	s_movk_i32 s13, 0x4000
	s_nop 0
	v_addc_co_u32_e32 v5, vcc, 0, v1, vcc
	global_load_dword v17, v[4:5], off nt
	v_add_co_u32_e32 v4, vcc, s13, v0
	s_movk_i32 s13, 0x3000
	s_nop 0
	v_addc_co_u32_e32 v5, vcc, 0, v1, vcc
	global_load_dword v18, v[4:5], off nt
	v_add_co_u32_e32 v4, vcc, s13, v0
	s_movk_i32 s13, 0x2000
	s_nop 0
	v_addc_co_u32_e32 v5, vcc, 0, v1, vcc
	global_load_dword v19, v[4:5], off nt
	v_add_co_u32_e32 v4, vcc, s13, v0
	s_movk_i32 s13, 0x1000
	s_nop 0
	v_addc_co_u32_e32 v5, vcc, 0, v1, vcc
	global_load_dword v21, v[4:5], off nt
	v_add_co_u32_e32 v4, vcc, s13, v0
	s_nop 1
	v_addc_co_u32_e32 v5, vcc, 0, v1, vcc
	global_load_dword v23, v[4:5], off nt
	global_load_dword v26, v138, s[2:3] nt
	s_mov_b32 s2, 0x20000
	v_add_co_u32_e32 v4, vcc, s2, v0
	s_mov_b32 s2, 0x1e000
	s_nop 0
	v_addc_co_u32_e32 v5, vcc, 0, v1, vcc
	v_add_co_u32_e32 v24, vcc, s2, v0
	s_mov_b32 s2, 0x1d000
	s_nop 0
	v_addc_co_u32_e32 v25, vcc, 0, v1, vcc
	global_load_dword v20, v[4:5], off offset:-4096 nt
	global_load_dword v22, v[24:25], off nt
	v_add_co_u32_e32 v24, vcc, s2, v0
	s_mov_b32 s2, 0x1c000
	s_nop 0
	v_addc_co_u32_e32 v25, vcc, 0, v1, vcc
	v_add_co_u32_e32 v28, vcc, s2, v0
	s_mov_b32 s2, 0x1b000
	s_nop 0
	v_addc_co_u32_e32 v29, vcc, 0, v1, vcc
	global_load_dword v24, v[24:25], off nt
	s_nop 0
	global_load_dword v25, v[28:29], off nt
	v_add_co_u32_e32 v28, vcc, s2, v0
	s_mov_b32 s2, 0x1a000
	s_nop 0
	v_addc_co_u32_e32 v29, vcc, 0, v1, vcc
	global_load_dword v27, v[28:29], off nt
	v_add_co_u32_e32 v28, vcc, s2, v0
	s_mov_b32 s2, 0x19000
	s_nop 0
	v_addc_co_u32_e32 v29, vcc, 0, v1, vcc
	v_add_co_u32_e32 v30, vcc, s2, v0
	global_load_dword v28, v[28:29], off nt
	s_nop 0
	v_addc_co_u32_e32 v31, vcc, 0, v1, vcc
	global_load_dword v29, v[30:31], off nt
	v_add_co_u32_e32 v30, vcc, 0x18000, v0
	s_mov_b32 s2, 0x17000
	s_nop 0
	v_addc_co_u32_e32 v31, vcc, 0, v1, vcc
	v_add_co_u32_e32 v32, vcc, s2, v0
	s_mov_b32 s2, 0x16000
	s_nop 0
	v_addc_co_u32_e32 v33, vcc, 0, v1, vcc
	global_load_dword v30, v[30:31], off nt
	s_nop 0
	global_load_dword v31, v[32:33], off nt
	v_add_co_u32_e32 v32, vcc, s2, v0
	s_mov_b32 s2, 0x15000
	s_nop 0
	v_addc_co_u32_e32 v33, vcc, 0, v1, vcc
	v_add_co_u32_e32 v34, vcc, s2, v0
	s_mov_b32 s2, 0x14000
	s_nop 0
	v_addc_co_u32_e32 v35, vcc, 0, v1, vcc
	global_load_dword v32, v[32:33], off nt
	s_nop 0
	global_load_dword v33, v[34:35], off nt
	v_add_co_u32_e32 v34, vcc, s2, v0
	s_mov_b32 s2, 0x13000
	s_nop 0
	v_addc_co_u32_e32 v35, vcc, 0, v1, vcc
	v_add_co_u32_e32 v36, vcc, s2, v0
	s_mov_b32 s2, 0x12000
	s_nop 0
	v_addc_co_u32_e32 v37, vcc, 0, v1, vcc
	v_add_co_u32_e32 v38, vcc, s2, v0
	s_mov_b32 s2, 0x11000
	s_nop 0
	v_addc_co_u32_e32 v39, vcc, 0, v1, vcc
	v_add_co_u32_e32 v40, vcc, s2, v0
	s_mov_b32 s2, 0x30000
	s_nop 0
	v_addc_co_u32_e32 v41, vcc, 0, v1, vcc
	global_load_dword v35, v[34:35], off nt
	s_nop 0
	global_load_dword v37, v[36:37], off nt
	s_nop 0
	global_load_dword v39, v[38:39], off nt
	s_nop 0
	global_load_dword v41, v[40:41], off nt
	s_nop 0
	global_load_dword v42, v[2:3], off nt
	v_add_co_u32_e32 v2, vcc, s2, v0
	s_mov_b32 s2, 0x2e000
	s_nop 0
	v_addc_co_u32_e32 v3, vcc, 0, v1, vcc
	v_add_co_u32_e32 v44, vcc, s2, v0
	s_mov_b32 s2, 0x2d000
	s_nop 0
	v_addc_co_u32_e32 v45, vcc, 0, v1, vcc
	global_load_dword v34, v[2:3], off offset:-4096 nt
	global_load_dword v36, v[44:45], off nt
	v_add_co_u32_e32 v44, vcc, s2, v0
	s_mov_b32 s2, 0x2c000
	s_nop 0
	v_addc_co_u32_e32 v45, vcc, 0, v1, vcc
	global_load_dword v38, v[44:45], off nt
	v_add_co_u32_e32 v44, vcc, s2, v0
	s_mov_b32 s2, 0x2b000
	s_nop 0
	v_addc_co_u32_e32 v45, vcc, 0, v1, vcc
	global_load_dword v40, v[44:45], off nt
	v_add_co_u32_e32 v44, vcc, s2, v0
	s_mov_b32 s2, 0x2a000
	s_nop 0
	v_addc_co_u32_e32 v45, vcc, 0, v1, vcc
	global_load_dword v43, v[44:45], off nt
	v_add_co_u32_e32 v44, vcc, s2, v0
	s_mov_b32 s2, 0x29000
	s_nop 0
	v_addc_co_u32_e32 v45, vcc, 0, v1, vcc
	v_add_co_u32_e32 v46, vcc, s2, v0
	s_mov_b32 s2, 0x28000
	s_nop 0
	v_addc_co_u32_e32 v47, vcc, 0, v1, vcc
	global_load_dword v44, v[44:45], off nt
	s_nop 0
	global_load_dword v45, v[46:47], off nt
	v_add_co_u32_e32 v46, vcc, s2, v0
	s_mov_b32 s2, 0x27000
	s_nop 0
	v_addc_co_u32_e32 v47, vcc, 0, v1, vcc
	v_add_co_u32_e32 v48, vcc, s2, v0
	s_mov_b32 s2, 0x26000
	s_nop 0
	v_addc_co_u32_e32 v49, vcc, 0, v1, vcc
	global_load_dword v46, v[46:47], off nt
	s_nop 0
	global_load_dword v47, v[48:49], off nt
	v_add_co_u32_e32 v48, vcc, s2, v0
	s_mov_b32 s2, 0x25000
	s_nop 0
	v_addc_co_u32_e32 v49, vcc, 0, v1, vcc
	v_add_co_u32_e32 v50, vcc, s2, v0
	s_mov_b32 s2, 0x24000
	s_nop 0
	v_addc_co_u32_e32 v51, vcc, 0, v1, vcc
	global_load_dword v48, v[48:49], off nt
	s_nop 0
	global_load_dword v49, v[50:51], off nt
	v_add_co_u32_e32 v50, vcc, s2, v0
	s_mov_b32 s2, 0x23000
	s_nop 0
	v_addc_co_u32_e32 v51, vcc, 0, v1, vcc
	v_add_co_u32_e32 v52, vcc, s2, v0
	s_mov_b32 s2, 0x22000
	s_nop 0
	v_addc_co_u32_e32 v53, vcc, 0, v1, vcc
	v_add_co_u32_e32 v54, vcc, s2, v0
	s_mov_b32 s2, 0x21000
	s_nop 0
	v_addc_co_u32_e32 v55, vcc, 0, v1, vcc
	v_add_co_u32_e32 v56, vcc, s2, v0
	s_mov_b32 s2, 0x40000
	s_nop 0
	v_addc_co_u32_e32 v57, vcc, 0, v1, vcc
	global_load_dword v51, v[50:51], off nt
	s_nop 0
	global_load_dword v53, v[52:53], off nt
	s_nop 0
	global_load_dword v55, v[54:55], off nt
	s_nop 0
	global_load_dword v57, v[56:57], off nt
	s_nop 0
	global_load_dword v58, v[4:5], off nt
	v_add_co_u32_e32 v4, vcc, s2, v0
	s_mov_b32 s2, 0x3e000
	s_nop 0
	v_addc_co_u32_e32 v5, vcc, 0, v1, vcc
	v_add_co_u32_e32 v60, vcc, s2, v0
	s_mov_b32 s2, 0x3d000
	s_nop 0
	v_addc_co_u32_e32 v61, vcc, 0, v1, vcc
	global_load_dword v50, v[4:5], off offset:-4096 nt
	global_load_dword v52, v[60:61], off nt
	v_add_co_u32_e32 v60, vcc, s2, v0
	s_mov_b32 s2, 0x3c000
	s_nop 0
	v_addc_co_u32_e32 v61, vcc, 0, v1, vcc
	global_load_dword v54, v[60:61], off nt
	v_add_co_u32_e32 v60, vcc, s2, v0
	s_mov_b32 s2, 0x3b000
	s_nop 0
	v_addc_co_u32_e32 v61, vcc, 0, v1, vcc
	global_load_dword v56, v[60:61], off nt
	v_add_co_u32_e32 v60, vcc, s2, v0
	s_mov_b32 s2, 0x3a000
	s_nop 0
	v_addc_co_u32_e32 v61, vcc, 0, v1, vcc
	global_load_dword v59, v[60:61], off nt
	v_add_co_u32_e32 v60, vcc, s2, v0
	s_mov_b32 s2, 0x39000
	s_nop 0
	v_addc_co_u32_e32 v61, vcc, 0, v1, vcc
	v_add_co_u32_e32 v62, vcc, s2, v0
	s_mov_b32 s2, 0x38000
	s_nop 0
	v_addc_co_u32_e32 v63, vcc, 0, v1, vcc
	global_load_dword v60, v[60:61], off nt
	s_nop 0
	global_load_dword v61, v[62:63], off nt
	v_add_co_u32_e32 v62, vcc, s2, v0
	s_mov_b32 s2, 0x37000
	s_nop 0
	v_addc_co_u32_e32 v63, vcc, 0, v1, vcc
	v_add_co_u32_e32 v64, vcc, s2, v0
	s_mov_b32 s2, 0x36000
	s_nop 0
	v_addc_co_u32_e32 v65, vcc, 0, v1, vcc
	global_load_dword v62, v[62:63], off nt
	s_nop 0
	global_load_dword v63, v[64:65], off nt
	v_add_co_u32_e32 v64, vcc, s2, v0
	s_mov_b32 s2, 0x35000
	s_nop 0
	v_addc_co_u32_e32 v65, vcc, 0, v1, vcc
	v_add_co_u32_e32 v66, vcc, s2, v0
	s_mov_b32 s2, 0x34000
	s_nop 0
	v_addc_co_u32_e32 v67, vcc, 0, v1, vcc
	global_load_dword v64, v[64:65], off nt
	s_nop 0
	global_load_dword v65, v[66:67], off nt
	v_add_co_u32_e32 v66, vcc, s2, v0
	s_mov_b32 s2, 0x33000
	s_nop 0
	v_addc_co_u32_e32 v67, vcc, 0, v1, vcc
	v_add_co_u32_e32 v68, vcc, s2, v0
	s_mov_b32 s2, 0x32000
	s_nop 0
	v_addc_co_u32_e32 v69, vcc, 0, v1, vcc
	v_add_co_u32_e32 v70, vcc, s2, v0
	s_mov_b32 s2, 0x31000
	s_nop 0
	v_addc_co_u32_e32 v71, vcc, 0, v1, vcc
	v_add_co_u32_e32 v72, vcc, s2, v0
	s_mov_b32 s2, 0x50000
	s_nop 0
	v_addc_co_u32_e32 v73, vcc, 0, v1, vcc
	global_load_dword v67, v[66:67], off nt
	s_nop 0
	global_load_dword v69, v[68:69], off nt
	s_nop 0
	global_load_dword v71, v[70:71], off nt
	s_nop 0
	global_load_dword v73, v[72:73], off nt
	s_nop 0
	global_load_dword v74, v[2:3], off nt
	v_add_co_u32_e32 v2, vcc, s2, v0
	s_mov_b32 s2, 0x4e000
	s_nop 0
	v_addc_co_u32_e32 v3, vcc, 0, v1, vcc
	v_add_co_u32_e32 v76, vcc, s2, v0
	s_mov_b32 s2, 0x4d000
	s_nop 0
	v_addc_co_u32_e32 v77, vcc, 0, v1, vcc
	global_load_dword v66, v[2:3], off offset:-4096 nt
	global_load_dword v68, v[76:77], off nt
	v_add_co_u32_e32 v76, vcc, s2, v0
	s_mov_b32 s2, 0x4c000
	s_nop 0
	v_addc_co_u32_e32 v77, vcc, 0, v1, vcc
	global_load_dword v70, v[76:77], off nt
	v_add_co_u32_e32 v76, vcc, s2, v0
	s_mov_b32 s2, 0x4b000
	s_nop 0
	v_addc_co_u32_e32 v77, vcc, 0, v1, vcc
	global_load_dword v72, v[76:77], off nt
	v_add_co_u32_e32 v76, vcc, s2, v0
	s_mov_b32 s2, 0x4a000
	s_nop 0
	v_addc_co_u32_e32 v77, vcc, 0, v1, vcc
	global_load_dword v75, v[76:77], off nt
	v_add_co_u32_e32 v76, vcc, s2, v0
	s_mov_b32 s2, 0x49000
	s_nop 0
	v_addc_co_u32_e32 v77, vcc, 0, v1, vcc
	v_add_co_u32_e32 v78, vcc, s2, v0
	s_mov_b32 s2, 0x48000
	s_nop 0
	v_addc_co_u32_e32 v79, vcc, 0, v1, vcc
	global_load_dword v76, v[76:77], off nt
	s_nop 0
	global_load_dword v77, v[78:79], off nt
	v_add_co_u32_e32 v78, vcc, s2, v0
	s_mov_b32 s2, 0x47000
	s_nop 0
	v_addc_co_u32_e32 v79, vcc, 0, v1, vcc
	v_add_co_u32_e32 v80, vcc, s2, v0
	s_mov_b32 s2, 0x46000
	s_nop 0
	v_addc_co_u32_e32 v81, vcc, 0, v1, vcc
	global_load_dword v78, v[78:79], off nt
	s_nop 0
	global_load_dword v79, v[80:81], off nt
	v_add_co_u32_e32 v80, vcc, s2, v0
	s_mov_b32 s2, 0x45000
	s_nop 0
	v_addc_co_u32_e32 v81, vcc, 0, v1, vcc
	v_add_co_u32_e32 v82, vcc, s2, v0
	s_mov_b32 s2, 0x44000
	s_nop 0
	v_addc_co_u32_e32 v83, vcc, 0, v1, vcc
	global_load_dword v80, v[80:81], off nt
	s_nop 0
	global_load_dword v81, v[82:83], off nt
	v_add_co_u32_e32 v82, vcc, s2, v0
	s_mov_b32 s2, 0x43000
	s_nop 0
	v_addc_co_u32_e32 v83, vcc, 0, v1, vcc
	v_add_co_u32_e32 v84, vcc, s2, v0
	s_mov_b32 s2, 0x42000
	s_nop 0
	v_addc_co_u32_e32 v85, vcc, 0, v1, vcc
	v_add_co_u32_e32 v86, vcc, s2, v0
	s_mov_b32 s2, 0x41000
	s_nop 0
	v_addc_co_u32_e32 v87, vcc, 0, v1, vcc
	v_add_co_u32_e32 v88, vcc, s2, v0
	s_mov_b32 s2, 0x60000
	s_nop 0
	v_addc_co_u32_e32 v89, vcc, 0, v1, vcc
	global_load_dword v83, v[82:83], off nt
	s_nop 0
	global_load_dword v85, v[84:85], off nt
	s_nop 0
	global_load_dword v87, v[86:87], off nt
	s_nop 0
	global_load_dword v89, v[88:89], off nt
	s_nop 0
	global_load_dword v90, v[4:5], off nt
	v_add_co_u32_e32 v4, vcc, s2, v0
	s_mov_b32 s2, 0x5e000
	s_nop 0
	v_addc_co_u32_e32 v5, vcc, 0, v1, vcc
	v_add_co_u32_e32 v92, vcc, s2, v0
	s_mov_b32 s2, 0x5d000
	s_nop 0
	v_addc_co_u32_e32 v93, vcc, 0, v1, vcc
	global_load_dword v82, v[4:5], off offset:-4096 nt
	global_load_dword v84, v[92:93], off nt
	v_add_co_u32_e32 v92, vcc, s2, v0
	s_mov_b32 s2, 0x5c000
	s_nop 0
	v_addc_co_u32_e32 v93, vcc, 0, v1, vcc
	global_load_dword v86, v[92:93], off nt
	v_add_co_u32_e32 v92, vcc, s2, v0
	s_mov_b32 s2, 0x5b000
	s_nop 0
	v_addc_co_u32_e32 v93, vcc, 0, v1, vcc
	global_load_dword v88, v[92:93], off nt
	v_add_co_u32_e32 v92, vcc, s2, v0
	s_mov_b32 s2, 0x5a000
	s_nop 0
	v_addc_co_u32_e32 v93, vcc, 0, v1, vcc
	global_load_dword v91, v[92:93], off nt
	v_add_co_u32_e32 v92, vcc, s2, v0
	s_mov_b32 s2, 0x59000
	s_nop 0
	v_addc_co_u32_e32 v93, vcc, 0, v1, vcc
	v_add_co_u32_e32 v94, vcc, s2, v0
	s_mov_b32 s2, 0x58000
	s_nop 0
	v_addc_co_u32_e32 v95, vcc, 0, v1, vcc
	global_load_dword v92, v[92:93], off nt
	s_nop 0
	global_load_dword v93, v[94:95], off nt
	v_add_co_u32_e32 v94, vcc, s2, v0
	s_mov_b32 s2, 0x57000
	s_nop 0
	v_addc_co_u32_e32 v95, vcc, 0, v1, vcc
	v_add_co_u32_e32 v98, vcc, s2, v0
	s_mov_b32 s2, 0x56000
	s_nop 0
	v_addc_co_u32_e32 v99, vcc, 0, v1, vcc
	global_load_dword v94, v[94:95], off nt
	s_nop 0
	global_load_dword v95, v[98:99], off nt
	v_add_co_u32_e32 v98, vcc, s2, v0
	s_mov_b32 s2, 0x55000
	s_nop 0
	v_addc_co_u32_e32 v99, vcc, 0, v1, vcc
	v_add_co_u32_e32 v100, vcc, s2, v0
	s_mov_b32 s2, 0x54000
	s_nop 0
	v_addc_co_u32_e32 v101, vcc, 0, v1, vcc
	global_load_dword v98, v[98:99], off nt
	s_nop 0
	global_load_dword v99, v[100:101], off nt
	v_add_co_u32_e32 v100, vcc, s2, v0
	s_mov_b32 s2, 0x53000
	s_nop 0
	v_addc_co_u32_e32 v101, vcc, 0, v1, vcc
	v_add_co_u32_e32 v102, vcc, s2, v0
	s_mov_b32 s2, 0x52000
	s_nop 0
	v_addc_co_u32_e32 v103, vcc, 0, v1, vcc
	global_load_dword v101, v[100:101], off nt
	s_nop 0
	global_load_dword v104, v[102:103], off nt
	v_add_co_u32_e32 v102, vcc, s2, v0
	s_mov_b32 s2, 0x51000
	s_nop 0
	v_addc_co_u32_e32 v103, vcc, 0, v1, vcc
	global_load_dword v105, v[102:103], off nt
	v_add_co_u32_e32 v102, vcc, s2, v0
	s_mov_b32 s2, 0x70000
	s_nop 0
	v_addc_co_u32_e32 v103, vcc, 0, v1, vcc
	global_load_dword v106, v[102:103], off nt
	global_load_dword v107, v[2:3], off nt
	v_add_co_u32_e32 v2, vcc, s2, v0
	s_mov_b32 s2, 0x6e000
	s_nop 0
	v_addc_co_u32_e32 v3, vcc, 0, v1, vcc
	v_add_co_u32_e32 v102, vcc, s2, v0
	s_mov_b32 s2, 0x6d000
	s_nop 0
	v_addc_co_u32_e32 v103, vcc, 0, v1, vcc
	global_load_dword v100, v[2:3], off offset:-4096 nt
	global_load_dword v108, v[102:103], off nt
	v_add_co_u32_e32 v102, vcc, s2, v0
	s_mov_b32 s2, 0x6c000
	s_nop 0
	v_addc_co_u32_e32 v103, vcc, 0, v1, vcc
	global_load_dword v109, v[102:103], off nt
	v_add_co_u32_e32 v102, vcc, s2, v0
	s_mov_b32 s2, 0x6b000
	s_nop 0
	v_addc_co_u32_e32 v103, vcc, 0, v1, vcc
	global_load_dword v110, v[102:103], off nt
	v_add_co_u32_e32 v102, vcc, s2, v0
	s_mov_b32 s2, 0x6a000
	s_nop 0
	v_addc_co_u32_e32 v103, vcc, 0, v1, vcc
	global_load_dword v111, v[102:103], off nt
	v_add_co_u32_e32 v102, vcc, s2, v0
	s_mov_b32 s2, 0x69000
	s_nop 0
	v_addc_co_u32_e32 v103, vcc, 0, v1, vcc
	global_load_dword v112, v[102:103], off nt
	v_add_co_u32_e32 v102, vcc, s2, v0
	s_mov_b32 s2, 0x68000
	s_nop 0
	v_addc_co_u32_e32 v103, vcc, 0, v1, vcc
	global_load_dword v113, v[102:103], off nt
	v_add_co_u32_e32 v102, vcc, s2, v0
	s_mov_b32 s2, 0x67000
	s_nop 0
	v_addc_co_u32_e32 v103, vcc, 0, v1, vcc
	global_load_dword v114, v[102:103], off nt
	v_add_co_u32_e32 v102, vcc, s2, v0
	s_mov_b32 s2, 0x66000
	s_nop 0
	v_addc_co_u32_e32 v103, vcc, 0, v1, vcc
	global_load_dword v115, v[102:103], off nt
	v_add_co_u32_e32 v102, vcc, s2, v0
	s_mov_b32 s2, 0x65000
	s_nop 0
	v_addc_co_u32_e32 v103, vcc, 0, v1, vcc
	global_load_dword v116, v[102:103], off nt
	v_add_co_u32_e32 v102, vcc, s2, v0
	s_mov_b32 s2, 0x64000
	s_nop 0
	v_addc_co_u32_e32 v103, vcc, 0, v1, vcc
	global_load_dword v117, v[102:103], off nt
	v_add_co_u32_e32 v102, vcc, s2, v0
	s_mov_b32 s2, 0x63000
	s_nop 0
	v_addc_co_u32_e32 v103, vcc, 0, v1, vcc
	global_load_dword v118, v[102:103], off nt
	v_add_co_u32_e32 v102, vcc, s2, v0
	s_mov_b32 s2, 0x62000
	s_nop 0
	v_addc_co_u32_e32 v103, vcc, 0, v1, vcc
	global_load_dword v119, v[102:103], off nt
	v_add_co_u32_e32 v102, vcc, s2, v0
	s_mov_b32 s2, 0x61000
	s_nop 0
	v_addc_co_u32_e32 v103, vcc, 0, v1, vcc
	global_load_dword v120, v[102:103], off nt
	v_add_co_u32_e32 v102, vcc, s2, v0
	s_mov_b32 s2, 0x7f000
	s_nop 0
	v_addc_co_u32_e32 v103, vcc, 0, v1, vcc
	global_load_dword v102, v[102:103], off nt
	s_nop 0
	global_load_dword v103, v[4:5], off nt
	v_add_co_u32_e32 v4, vcc, s2, v0
	s_mov_b32 s2, 0x7e000
	s_nop 0
	v_addc_co_u32_e32 v5, vcc, 0, v1, vcc
	global_load_dword v121, v[4:5], off nt
	v_add_co_u32_e32 v4, vcc, s2, v0
	s_mov_b32 s2, 0x7d000
	s_nop 0
	v_addc_co_u32_e32 v5, vcc, 0, v1, vcc
	global_load_dword v122, v[4:5], off nt
	v_add_co_u32_e32 v4, vcc, s2, v0
	s_mov_b32 s2, 0x7c000
	s_nop 0
	v_addc_co_u32_e32 v5, vcc, 0, v1, vcc
	global_load_dword v123, v[4:5], off nt
	v_add_co_u32_e32 v4, vcc, s2, v0
	s_mov_b32 s2, 0x7b000
	s_nop 0
	v_addc_co_u32_e32 v5, vcc, 0, v1, vcc
	global_load_dword v124, v[4:5], off nt
	v_add_co_u32_e32 v4, vcc, s2, v0
	s_mov_b32 s2, 0x7a000
	s_nop 0
	v_addc_co_u32_e32 v5, vcc, 0, v1, vcc
	global_load_dword v125, v[4:5], off nt
	v_add_co_u32_e32 v4, vcc, s2, v0
	s_mov_b32 s2, 0x79000
	s_nop 0
	v_addc_co_u32_e32 v5, vcc, 0, v1, vcc
	global_load_dword v126, v[4:5], off nt
	v_add_co_u32_e32 v4, vcc, s2, v0
	s_mov_b32 s2, 0x78000
	s_nop 0
	v_addc_co_u32_e32 v5, vcc, 0, v1, vcc
	global_load_dword v127, v[4:5], off nt
	v_add_co_u32_e32 v4, vcc, s2, v0
	s_mov_b32 s2, 0x77000
	s_nop 0
	v_addc_co_u32_e32 v5, vcc, 0, v1, vcc
	global_load_dword v128, v[4:5], off nt
	v_add_co_u32_e32 v4, vcc, s2, v0
	s_mov_b32 s2, 0x76000
	s_nop 0
	v_addc_co_u32_e32 v5, vcc, 0, v1, vcc
	global_load_dword v129, v[4:5], off nt
	v_add_co_u32_e32 v4, vcc, s2, v0
	s_mov_b32 s2, 0x75000
	s_nop 0
	v_addc_co_u32_e32 v5, vcc, 0, v1, vcc
	global_load_dword v130, v[4:5], off nt
	v_add_co_u32_e32 v4, vcc, s2, v0
	s_mov_b32 s2, 0x74000
	s_nop 0
	v_addc_co_u32_e32 v5, vcc, 0, v1, vcc
	global_load_dword v131, v[4:5], off nt
	v_add_co_u32_e32 v4, vcc, s2, v0
	s_mov_b32 s2, 0x73000
	s_nop 0
	v_addc_co_u32_e32 v5, vcc, 0, v1, vcc
	global_load_dword v132, v[4:5], off nt
	v_add_co_u32_e32 v4, vcc, s2, v0
	s_mov_b32 s2, 0x72000
	s_nop 0
	v_addc_co_u32_e32 v5, vcc, 0, v1, vcc
	global_load_dword v133, v[4:5], off nt
	v_add_co_u32_e32 v4, vcc, s2, v0
	s_mov_b32 s2, 0x71000
	s_nop 0
	v_addc_co_u32_e32 v5, vcc, 0, v1, vcc
	v_add_co_u32_e32 v0, vcc, s2, v0
	global_load_dword v4, v[4:5], off nt
	s_nop 0
	v_addc_co_u32_e32 v1, vcc, 0, v1, vcc
	global_load_dword v5, v[0:1], off nt
	global_load_dword v134, v[2:3], off nt
	v_mov_b32_e32 v0, s18
	s_movk_i32 s2, 0x90
	s_waitcnt vmcnt(62)
	v_mad_u32_u24 v135, v6, s2, v0
	v_mul_f32_e32 v1, 0x42800000, v26
	v_mul_f32_e32 v2, 0x42800000, v23
	v_mov_b32_e32 v0, v97
	v_cvt_pk_fp8_f32 v0, v1, v2
	v_mul_f32_e32 v3, 0x42800000, v21
	v_mul_f32_e32 v19, 0x42800000, v19
	v_mul_f32_e32 v2, 0x42800000, v18
	v_cvt_pk_fp8_f32 v0, v3, v19 op_sel:[0,0,1]
	v_mul_f32_e32 v3, 0x42800000, v17
	v_mov_b32_e32 v1, v97
	v_cvt_pk_fp8_f32 v1, v2, v3
	v_mul_f32_e32 v3, 0x42800000, v14
	v_mul_f32_e32 v13, 0x42800000, v13
	v_mov_b32_e32 v2, v97
	v_cvt_pk_fp8_f32 v2, v3, v13
	v_mul_f32_e32 v10, 0x42800000, v10
	v_mul_f32_e32 v9, 0x42800000, v9
	v_mov_b32_e32 v3, v97
	v_cvt_pk_fp8_f32 v3, v10, v9
	v_mul_f32_e32 v16, 0x42800000, v16
	v_mul_f32_e32 v15, 0x42800000, v15
	v_mul_f32_e32 v12, 0x42800000, v12
	v_mul_f32_e32 v11, 0x42800000, v11
	v_mul_f32_e32 v8, 0x42800000, v8
	v_mul_f32_e32 v7, 0x42800000, v7
	v_cvt_pk_fp8_f32 v1, v16, v15 op_sel:[0,0,1]
	v_cvt_pk_fp8_f32 v2, v12, v11 op_sel:[0,0,1]
	v_cvt_pk_fp8_f32 v3, v8, v7 op_sel:[0,0,1]
	s_waitcnt vmcnt(48)
	s_waitcnt vmcnt(32)
	s_waitcnt vmcnt(16)
	s_waitcnt vmcnt(0)
	ds_write_b128 v135, v[0:3]
	v_mul_f32_e32 v1, 0x42800000, v42
	v_mul_f32_e32 v2, 0x42800000, v41
	v_mov_b32_e32 v0, v97
	v_cvt_pk_fp8_f32 v0, v1, v2
	v_mul_f32_e32 v3, 0x42800000, v39
	v_mul_f32_e32 v7, 0x42800000, v37
	v_mul_f32_e32 v2, 0x42800000, v35
	v_cvt_pk_fp8_f32 v0, v3, v7 op_sel:[0,0,1]
	v_mul_f32_e32 v3, 0x42800000, v33
	v_mov_b32_e32 v1, v97
	v_cvt_pk_fp8_f32 v1, v2, v3
	v_mul_f32_e32 v7, 0x42800000, v32
	v_mul_f32_e32 v8, 0x42800000, v31
	v_mul_f32_e32 v3, 0x42800000, v30
	v_cvt_pk_fp8_f32 v1, v7, v8 op_sel:[0,0,1]
	v_mul_f32_e32 v7, 0x42800000, v29
	v_mov_b32_e32 v2, v97
	v_cvt_pk_fp8_f32 v2, v3, v7
	v_mul_f32_e32 v8, 0x42800000, v28
	v_mul_f32_e32 v9, 0x42800000, v27
	v_mul_f32_e32 v7, 0x42800000, v25
	v_cvt_pk_fp8_f32 v2, v8, v9 op_sel:[0,0,1]
	v_mul_f32_e32 v8, 0x42800000, v24
	v_mov_b32_e32 v3, v97
	v_cvt_pk_fp8_f32 v3, v7, v8
	v_mul_f32_e32 v9, 0x42800000, v22
	v_mul_f32_e32 v10, 0x42800000, v20
	v_mul_f32_e32 v7, 0x42800000, v53
	v_cvt_pk_fp8_f32 v3, v9, v10 op_sel:[0,0,1]
	v_mul_f32_e32 v8, 0x42800000, v47
	v_mul_f32_e32 v9, 0x42800000, v43
	v_mul_f32_e32 v10, 0x42800000, v34
	ds_write_b128 v135, v[0:3] offset:16
	v_mul_f32_e32 v1, 0x42800000, v58
	v_mul_f32_e32 v2, 0x42800000, v57
	v_mov_b32_e32 v0, v97
	v_cvt_pk_fp8_f32 v0, v1, v2
	v_mul_f32_e32 v3, 0x42800000, v55
	v_mul_f32_e32 v2, 0x42800000, v51
	v_mov_b32_e32 v1, v97
	v_cvt_pk_fp8_f32 v0, v3, v7 op_sel:[0,0,1]
	v_mul_f32_e32 v3, 0x42800000, v49
	v_cvt_pk_fp8_f32 v1, v2, v3
	v_mul_f32_e32 v7, 0x42800000, v48
	v_mul_f32_e32 v3, 0x42800000, v46
	v_mov_b32_e32 v2, v97
	v_cvt_pk_fp8_f32 v1, v7, v8 op_sel:[0,0,1]
	v_mul_f32_e32 v7, 0x42800000, v45
	v_cvt_pk_fp8_f32 v2, v3, v7
	v_mul_f32_e32 v8, 0x42800000, v44
	v_mul_f32_e32 v7, 0x42800000, v40
	v_mov_b32_e32 v3, v97
	v_cvt_pk_fp8_f32 v2, v8, v9 op_sel:[0,0,1]
	v_mul_f32_e32 v8, 0x42800000, v38
	v_cvt_pk_fp8_f32 v3, v7, v8
	v_mul_f32_e32 v9, 0x42800000, v36
	v_mul_f32_e32 v7, 0x42800000, v69
	v_mul_f32_e32 v8, 0x42800000, v63
	v_cvt_pk_fp8_f32 v3, v9, v10 op_sel:[0,0,1]
	v_mul_f32_e32 v9, 0x42800000, v59
	v_mul_f32_e32 v10, 0x42800000, v50
	s_add_u32 s2, s24, s12
	ds_write_b128 v135, v[0:3] offset:32
	v_mul_f32_e32 v1, 0x42800000, v74
	v_mul_f32_e32 v2, 0x42800000, v73
	v_mov_b32_e32 v0, v97
	v_cvt_pk_fp8_f32 v0, v1, v2
	v_mul_f32_e32 v3, 0x42800000, v71
	v_mul_f32_e32 v2, 0x42800000, v67
	v_mov_b32_e32 v1, v97
	v_cvt_pk_fp8_f32 v0, v3, v7 op_sel:[0,0,1]
	v_mul_f32_e32 v3, 0x42800000, v65
	v_cvt_pk_fp8_f32 v1, v2, v3
	v_mul_f32_e32 v7, 0x42800000, v64
	v_mul_f32_e32 v3, 0x42800000, v62
	v_mov_b32_e32 v2, v97
	v_cvt_pk_fp8_f32 v1, v7, v8 op_sel:[0,0,1]
	v_mul_f32_e32 v7, 0x42800000, v61
	v_cvt_pk_fp8_f32 v2, v3, v7
	v_mul_f32_e32 v8, 0x42800000, v60
	v_mul_f32_e32 v7, 0x42800000, v56
	v_mov_b32_e32 v3, v97
	v_cvt_pk_fp8_f32 v2, v8, v9 op_sel:[0,0,1]
	v_mul_f32_e32 v8, 0x42800000, v54
	v_cvt_pk_fp8_f32 v3, v7, v8
	v_mul_f32_e32 v9, 0x42800000, v52
	v_mul_f32_e32 v7, 0x42800000, v85
	v_mul_f32_e32 v8, 0x42800000, v79
	v_cvt_pk_fp8_f32 v3, v9, v10 op_sel:[0,0,1]
	v_mul_f32_e32 v9, 0x42800000, v75
	v_mul_f32_e32 v10, 0x42800000, v66
	s_addc_u32 s3, s25, 0
	ds_write_b128 v135, v[0:3] offset:48
	v_mul_f32_e32 v1, 0x42800000, v90
	v_mul_f32_e32 v2, 0x42800000, v89
	v_mov_b32_e32 v0, v97
	v_cvt_pk_fp8_f32 v0, v1, v2
	v_mul_f32_e32 v3, 0x42800000, v87
	v_mul_f32_e32 v2, 0x42800000, v83
	v_mov_b32_e32 v1, v97
	v_cvt_pk_fp8_f32 v0, v3, v7 op_sel:[0,0,1]
	v_mul_f32_e32 v3, 0x42800000, v81
	v_cvt_pk_fp8_f32 v1, v2, v3
	v_mul_f32_e32 v7, 0x42800000, v80
	v_mul_f32_e32 v3, 0x42800000, v78
	v_mov_b32_e32 v2, v97
	v_cvt_pk_fp8_f32 v1, v7, v8 op_sel:[0,0,1]
	v_mul_f32_e32 v7, 0x42800000, v77
	v_cvt_pk_fp8_f32 v2, v3, v7
	v_mul_f32_e32 v8, 0x42800000, v76
	v_mul_f32_e32 v7, 0x42800000, v72
	v_mov_b32_e32 v3, v97
	v_cvt_pk_fp8_f32 v2, v8, v9 op_sel:[0,0,1]
	v_mul_f32_e32 v8, 0x42800000, v70
	v_cvt_pk_fp8_f32 v3, v7, v8
	v_mul_f32_e32 v9, 0x42800000, v68
	v_mul_f32_e32 v7, 0x42800000, v104
	v_mul_f32_e32 v8, 0x42800000, v95
	v_cvt_pk_fp8_f32 v3, v9, v10 op_sel:[0,0,1]
	v_mul_f32_e32 v9, 0x42800000, v91
	v_mul_f32_e32 v10, 0x42800000, v82
	ds_write_b128 v135, v[0:3] offset:64
	v_mul_f32_e32 v1, 0x42800000, v107
	v_mul_f32_e32 v2, 0x42800000, v106
	v_mov_b32_e32 v0, v97
	v_cvt_pk_fp8_f32 v0, v1, v2
	v_mul_f32_e32 v3, 0x42800000, v105
	v_mul_f32_e32 v2, 0x42800000, v101
	v_mov_b32_e32 v1, v97
	v_cvt_pk_fp8_f32 v0, v3, v7 op_sel:[0,0,1]
	v_mul_f32_e32 v3, 0x42800000, v99
	v_cvt_pk_fp8_f32 v1, v2, v3
	v_mul_f32_e32 v7, 0x42800000, v98
	v_mul_f32_e32 v3, 0x42800000, v94
	v_mov_b32_e32 v2, v97
	v_cvt_pk_fp8_f32 v1, v7, v8 op_sel:[0,0,1]
	v_mul_f32_e32 v7, 0x42800000, v93
	v_cvt_pk_fp8_f32 v2, v3, v7
	v_mul_f32_e32 v8, 0x42800000, v92
	v_mul_f32_e32 v7, 0x42800000, v88
	v_mov_b32_e32 v3, v97
	v_cvt_pk_fp8_f32 v2, v8, v9 op_sel:[0,0,1]
	v_mul_f32_e32 v8, 0x42800000, v86
	v_cvt_pk_fp8_f32 v3, v7, v8
	v_mul_f32_e32 v9, 0x42800000, v84
	v_mul_f32_e32 v7, 0x42800000, v119
	v_mul_f32_e32 v8, 0x42800000, v115
	v_cvt_pk_fp8_f32 v3, v9, v10 op_sel:[0,0,1]
	v_mul_f32_e32 v9, 0x42800000, v111
	v_mul_f32_e32 v10, 0x42800000, v100
	ds_write_b128 v135, v[0:3] offset:80
	v_mul_f32_e32 v1, 0x42800000, v103
	v_mul_f32_e32 v2, 0x42800000, v102
	v_mov_b32_e32 v0, v97
	v_cvt_pk_fp8_f32 v0, v1, v2
	v_mul_f32_e32 v3, 0x42800000, v120
	v_mul_f32_e32 v2, 0x42800000, v118
	v_mov_b32_e32 v1, v97
	v_cvt_pk_fp8_f32 v0, v3, v7 op_sel:[0,0,1]
	v_mul_f32_e32 v3, 0x42800000, v117
	v_cvt_pk_fp8_f32 v1, v2, v3
	v_mul_f32_e32 v7, 0x42800000, v116
	v_mul_f32_e32 v3, 0x42800000, v114
	v_mov_b32_e32 v2, v97
	v_cvt_pk_fp8_f32 v1, v7, v8 op_sel:[0,0,1]
	v_mul_f32_e32 v7, 0x42800000, v113
	v_cvt_pk_fp8_f32 v2, v3, v7
	v_mul_f32_e32 v8, 0x42800000, v112
	v_mul_f32_e32 v7, 0x42800000, v110
	v_mov_b32_e32 v3, v97
	v_cvt_pk_fp8_f32 v2, v8, v9 op_sel:[0,0,1]
	v_mul_f32_e32 v8, 0x42800000, v109
	v_cvt_pk_fp8_f32 v3, v7, v8
	v_mul_f32_e32 v9, 0x42800000, v108
	v_mul_f32_e32 v7, 0x42800000, v125
	v_mul_f32_e32 v8, 0x42800000, v121
	v_cvt_pk_fp8_f32 v3, v9, v10 op_sel:[0,0,1]
	v_mov_b32_e32 v9, v97
	ds_write_b128 v135, v[0:3] offset:96
	v_mul_f32_e32 v1, 0x42800000, v134
	v_mul_f32_e32 v2, 0x42800000, v5
	v_mov_b32_e32 v0, v97
	v_cvt_pk_fp8_f32 v0, v1, v2
	v_mul_f32_e32 v3, 0x42800000, v4
	v_mul_f32_e32 v4, 0x42800000, v133
	v_mul_f32_e32 v2, 0x42800000, v132
	v_cvt_pk_fp8_f32 v0, v3, v4 op_sel:[0,0,1]
	v_mul_f32_e32 v3, 0x42800000, v131
	v_mov_b32_e32 v1, v97
	v_cvt_pk_fp8_f32 v1, v2, v3
	v_mul_f32_e32 v4, 0x42800000, v130
	v_mul_f32_e32 v5, 0x42800000, v129
	v_mul_f32_e32 v3, 0x42800000, v128
	v_cvt_pk_fp8_f32 v1, v4, v5 op_sel:[0,0,1]
	v_mul_f32_e32 v4, 0x42800000, v127
	v_mov_b32_e32 v2, v97
	v_cvt_pk_fp8_f32 v2, v3, v4
	v_mul_f32_e32 v5, 0x42800000, v126
	v_mul_f32_e32 v4, 0x42800000, v124
	v_mov_b32_e32 v3, v97
	v_cvt_pk_fp8_f32 v2, v5, v7 op_sel:[0,0,1]
	v_mul_f32_e32 v5, 0x42800000, v123
	v_cvt_pk_fp8_f32 v3, v4, v5
	v_mul_f32_e32 v7, 0x42800000, v122
	v_cvt_pk_fp8_f32 v3, v7, v8 op_sel:[0,0,1]
	v_lshrrev_b32_e32 v8, 3, v6
	ds_write_b128 v135, v[0:3] offset:112
	v_lshlrev_b32_e32 v0, 4, v6
	v_and_b32_e32 v0, 0x70, v0
	v_mov_b32_e32 v1, v97
	v_lshl_add_u64 v[2:3], s[2:3], 0, v[0:1]
	v_mul_u32_u24_e32 v1, 0x90, v8
	s_waitcnt lgkmcnt(0)
	s_mov_b64 s[2:3], 0x23b00000
	v_add3_u32 v7, s18, v0, v1
	v_lshl_add_u64 v[4:5], v[2:3], 0, s[2:3]
	ds_read_b128 v[0:3], v7
	v_or_b32_e32 v8, s21, v8
	v_lshlrev_b32_e32 v8, 10, v8
	v_lshl_add_u64 v[10:11], v[4:5], 0, v[8:9]
	s_mov_b64 s[2:3], 0
	s_waitcnt lgkmcnt(0)
	global_store_dwordx4 v[10:11], v[0:3], off
	ds_read_b128 v[0:3], v7 offset:1152
	v_or_b32_e32 v10, 0x2000, v8
	v_mov_b32_e32 v11, v97
	v_lshl_add_u64 v[10:11], v[4:5], 0, v[10:11]
	s_waitcnt lgkmcnt(0)
	global_store_dwordx4 v[10:11], v[0:3], off
	ds_read_b128 v[0:3], v7 offset:2304
	v_or_b32_e32 v10, 0x4000, v8
	v_mov_b32_e32 v11, v97
	v_lshl_add_u64 v[10:11], v[4:5], 0, v[10:11]
	s_waitcnt lgkmcnt(0)
	global_store_dwordx4 v[10:11], v[0:3], off
	ds_read_b128 v[0:3], v7 offset:3456
	v_or_b32_e32 v10, 0x6000, v8
	v_mov_b32_e32 v11, v97
	v_lshl_add_u64 v[10:11], v[4:5], 0, v[10:11]
	s_waitcnt lgkmcnt(0)
	global_store_dwordx4 v[10:11], v[0:3], off
	ds_read_b128 v[0:3], v7 offset:4608
	v_or_b32_e32 v10, 0x8000, v8
	v_mov_b32_e32 v11, v97
	v_lshl_add_u64 v[10:11], v[4:5], 0, v[10:11]
	s_waitcnt lgkmcnt(0)
	global_store_dwordx4 v[10:11], v[0:3], off
	ds_read_b128 v[0:3], v7 offset:5760
	v_or_b32_e32 v10, 0xa000, v8
	v_mov_b32_e32 v11, v97
	v_lshl_add_u64 v[10:11], v[4:5], 0, v[10:11]
	s_waitcnt lgkmcnt(0)
	global_store_dwordx4 v[10:11], v[0:3], off
	ds_read_b128 v[0:3], v7 offset:6912
	v_or_b32_e32 v10, 0xc000, v8
	v_mov_b32_e32 v11, v97
	v_lshl_add_u64 v[10:11], v[4:5], 0, v[10:11]
	v_or_b32_e32 v8, 0xe000, v8
	s_waitcnt lgkmcnt(0)
	global_store_dwordx4 v[10:11], v[0:3], off
	ds_read_b128 v[0:3], v7 offset:8064
	v_lshl_add_u64 v[4:5], v[4:5], 0, v[8:9]
	s_waitcnt lgkmcnt(0)
	global_store_dwordx4 v[4:5], v[0:3], off
	s_waitcnt lgkmcnt(0)
.Lc3_1477:
	s_andn2_b64 vcc, exec, s[2:3]
	s_cbranch_vccnz .Lc3_done
	s_ashr_i32 s21, s19, 8
	s_load_dwordx2 s[2:3], s[22:23], 0x60
	s_lshl_b32 s20, s20, 5
	s_ashr_i32 s22, s21, 31
	s_add_u32 s20, s21, s20
	s_addc_u32 s21, s22, 0
	s_lshl_b64 s[22:23], s[20:21], 23
	s_waitcnt lgkmcnt(0)
	s_add_u32 s25, s2, s22
	s_addc_u32 s12, s3, s23
	s_lshl_b64 s[2:3], s[20:21], 21
	s_add_u32 s21, s16, s2
	s_addc_u32 s22, s17, s3
	s_lshl_b32 s2, s19, 2
	s_and_b32 s23, s2, 0x380
	s_lshl_b32 s24, s19, 6
	s_and_b32 s20, s24, 0x3fc0
	s_lshl_b32 s2, s23, 13
	s_add_u32 s2, s25, s2
	s_addc_u32 s3, s12, 0
	s_lshl_b32 s19, s19, 8
	s_and_b32 s19, s19, 0x1f00
	s_add_u32 s2, s2, s19
	s_addc_u32 s3, s3, 0
	v_lshl_add_u64 v[0:1], s[2:3], 0, v[138:139]
	s_mov_b32 s19, 0x1e000
	v_add_co_u32_e32 v2, vcc, s19, v0
	s_mov_b32 s19, 0x1c000
	s_nop 0
	v_addc_co_u32_e32 v3, vcc, 0, v1, vcc
	v_add_co_u32_e32 v4, vcc, s19, v0
	s_mov_b32 s19, 0x1a000
	s_nop 0
	v_addc_co_u32_e32 v5, vcc, 0, v1, vcc
	global_load_dword v2, v[2:3], off nt
	v_mov_b32_e32 v102, v97
	global_load_dword v3, v[4:5], off nt
	v_add_co_u32_e32 v4, vcc, s19, v0
	s_mov_b32 s19, 0x16000
	s_nop 0
	v_addc_co_u32_e32 v5, vcc, 0, v1, vcc
	v_add_co_u32_e32 v8, vcc, 0x18000, v0
	global_load_dword v4, v[4:5], off nt
	s_nop 0
	v_addc_co_u32_e32 v9, vcc, 0, v1, vcc
	global_load_dword v5, v[8:9], off nt
	v_add_co_u32_e32 v8, vcc, s19, v0
	s_mov_b32 s19, 0x14000
	s_nop 0
	v_addc_co_u32_e32 v9, vcc, 0, v1, vcc
	global_load_dword v7, v[8:9], off nt
	v_add_co_u32_e32 v8, vcc, s19, v0
	s_mov_b32 s19, 0x12000
	s_nop 0
	v_addc_co_u32_e32 v9, vcc, 0, v1, vcc
	v_add_co_u32_e32 v10, vcc, s19, v0
	s_mov_b32 s19, 0x10000
	s_nop 0
	v_addc_co_u32_e32 v11, vcc, 0, v1, vcc
	global_load_dword v8, v[8:9], off nt
	v_mov_b32_e32 v103, v97
	global_load_dword v9, v[10:11], off nt
	v_add_co_u32_e32 v10, vcc, s19, v0
	s_mov_b32 s19, 0xe000
	s_nop 0
	v_addc_co_u32_e32 v11, vcc, 0, v1, vcc
	v_add_co_u32_e32 v12, vcc, s19, v0
	s_mov_b32 s19, 0xc000
	s_nop 0
	v_addc_co_u32_e32 v13, vcc, 0, v1, vcc
	global_load_dword v10, v[10:11], off nt
	s_nop 0
	global_load_dword v11, v[12:13], off nt
	v_add_co_u32_e32 v12, vcc, s19, v0
	s_mov_b32 s19, 0xa000
	s_nop 0
	v_addc_co_u32_e32 v13, vcc, 0, v1, vcc
	v_add_co_u32_e32 v14, vcc, s19, v0
	s_mov_b32 s19, 0x8000
	s_nop 0
	v_addc_co_u32_e32 v15, vcc, 0, v1, vcc
	global_load_dword v12, v[12:13], off nt
	s_nop 0
	global_load_dword v13, v[14:15], off nt
	v_add_co_u32_e32 v14, vcc, s19, v0
	s_movk_i32 s19, 0x6000
	s_nop 0
	v_addc_co_u32_e32 v15, vcc, 0, v1, vcc
	v_add_co_u32_e32 v16, vcc, s19, v0
	s_movk_i32 s19, 0x4000
	s_nop 0
	v_addc_co_u32_e32 v17, vcc, 0, v1, vcc
	v_add_co_u32_e32 v18, vcc, s19, v0
	s_movk_i32 s19, 0x2000
	s_nop 0
	v_addc_co_u32_e32 v19, vcc, 0, v1, vcc
	v_add_co_u32_e32 v20, vcc, s19, v0
	global_load_dword v15, v[14:15], off nt
	s_nop 0
	v_addc_co_u32_e32 v21, vcc, 0, v1, vcc
	global_load_dword v17, v[16:17], off nt
	s_nop 0
	global_load_dword v19, v[18:19], off nt
	s_nop 0
	global_load_dword v21, v[20:21], off nt
	s_nop 0
	global_load_dword v22, v138, s[2:3] nt
	s_mov_b32 s2, 0x3e000
	v_add_co_u32_e32 v24, vcc, s2, v0
	s_mov_b32 s2, 0x3c000
	s_nop 0
	v_addc_co_u32_e32 v25, vcc, 0, v1, vcc
	global_load_dword v14, v[24:25], off nt
	v_add_co_u32_e32 v24, vcc, s2, v0
	s_mov_b32 s2, 0x3a000
	s_nop 0
	v_addc_co_u32_e32 v25, vcc, 0, v1, vcc
	global_load_dword v16, v[24:25], off nt
	v_add_co_u32_e32 v24, vcc, s2, v0
	s_mov_b32 s2, 0x38000
	s_nop 0
	v_addc_co_u32_e32 v25, vcc, 0, v1, vcc
	global_load_dword v18, v[24:25], off nt
	v_add_co_u32_e32 v24, vcc, s2, v0
	s_mov_b32 s2, 0x36000
	s_nop 0
	v_addc_co_u32_e32 v25, vcc, 0, v1, vcc
	global_load_dword v20, v[24:25], off nt
	v_add_co_u32_e32 v24, vcc, s2, v0
	s_mov_b32 s2, 0x34000
	s_nop 0
	v_addc_co_u32_e32 v25, vcc, 0, v1, vcc
	global_load_dword v23, v[24:25], off nt
	v_add_co_u32_e32 v24, vcc, s2, v0
	s_mov_b32 s2, 0x32000
	s_nop 0
	v_addc_co_u32_e32 v25, vcc, 0, v1, vcc
	v_add_co_u32_e32 v26, vcc, s2, v0
	s_mov_b32 s2, 0x30000
	s_nop 0
	v_addc_co_u32_e32 v27, vcc, 0, v1, vcc
	global_load_dword v24, v[24:25], off nt
	s_nop 0
	global_load_dword v25, v[26:27], off nt
	v_add_co_u32_e32 v26, vcc, s2, v0
	s_mov_b32 s2, 0x2e000
	s_nop 0
	v_addc_co_u32_e32 v27, vcc, 0, v1, vcc
	v_add_co_u32_e32 v28, vcc, s2, v0
	s_mov_b32 s2, 0x2c000
	s_nop 0
	v_addc_co_u32_e32 v29, vcc, 0, v1, vcc
	global_load_dword v26, v[26:27], off nt
	s_nop 0
	global_load_dword v27, v[28:29], off nt
	v_add_co_u32_e32 v28, vcc, s2, v0
	s_mov_b32 s2, 0x2a000
	s_nop 0
	v_addc_co_u32_e32 v29, vcc, 0, v1, vcc
	v_add_co_u32_e32 v30, vcc, s2, v0
	s_mov_b32 s2, 0x28000
	s_nop 0
	v_addc_co_u32_e32 v31, vcc, 0, v1, vcc
	global_load_dword v28, v[28:29], off nt
	s_nop 0
	global_load_dword v29, v[30:31], off nt
	v_add_co_u32_e32 v30, vcc, s2, v0
	s_mov_b32 s2, 0x26000
	s_nop 0
	v_addc_co_u32_e32 v31, vcc, 0, v1, vcc
	v_add_co_u32_e32 v32, vcc, s2, v0
	s_mov_b32 s2, 0x24000
	s_nop 0
	v_addc_co_u32_e32 v33, vcc, 0, v1, vcc
	v_add_co_u32_e32 v34, vcc, s2, v0
	s_mov_b32 s2, 0x22000
	s_nop 0
	v_addc_co_u32_e32 v35, vcc, 0, v1, vcc
	v_add_co_u32_e32 v36, vcc, s2, v0
	s_mov_b32 s2, 0x20000
	s_nop 0
	v_addc_co_u32_e32 v37, vcc, 0, v1, vcc
	v_add_co_u32_e32 v38, vcc, s2, v0
	s_mov_b32 s2, 0x5e000
	s_nop 0
	v_addc_co_u32_e32 v39, vcc, 0, v1, vcc
	v_add_co_u32_e32 v40, vcc, s2, v0
	s_mov_b32 s2, 0x5c000
	s_nop 0
	v_addc_co_u32_e32 v41, vcc, 0, v1, vcc
	global_load_dword v30, v[30:31], off nt
	s_nop 0
	global_load_dword v32, v[32:33], off nt
	s_nop 0
	global_load_dword v34, v[34:35], off nt
	s_nop 0
	global_load_dword v36, v[36:37], off nt
	s_nop 0
	global_load_dword v38, v[38:39], off nt
	s_nop 0
	global_load_dword v31, v[40:41], off nt
	v_add_co_u32_e32 v40, vcc, s2, v0
	s_mov_b32 s2, 0x5a000
	s_nop 0
	v_addc_co_u32_e32 v41, vcc, 0, v1, vcc
	global_load_dword v33, v[40:41], off nt
	v_add_co_u32_e32 v40, vcc, s2, v0
	s_mov_b32 s2, 0x58000
	s_nop 0
	v_addc_co_u32_e32 v41, vcc, 0, v1, vcc
	global_load_dword v35, v[40:41], off nt
	v_add_co_u32_e32 v40, vcc, s2, v0
	s_mov_b32 s2, 0x56000
	s_nop 0
	v_addc_co_u32_e32 v41, vcc, 0, v1, vcc
	global_load_dword v37, v[40:41], off nt
	v_add_co_u32_e32 v40, vcc, s2, v0
	s_mov_b32 s2, 0x54000
	s_nop 0
	v_addc_co_u32_e32 v41, vcc, 0, v1, vcc
	global_load_dword v39, v[40:41], off nt
	v_add_co_u32_e32 v40, vcc, s2, v0
	s_mov_b32 s2, 0x52000
	s_nop 0
	v_addc_co_u32_e32 v41, vcc, 0, v1, vcc
	v_add_co_u32_e32 v42, vcc, s2, v0
	s_mov_b32 s2, 0x50000
	s_nop 0
	v_addc_co_u32_e32 v43, vcc, 0, v1, vcc
	global_load_dword v40, v[40:41], off nt
	s_nop 0
	global_load_dword v41, v[42:43], off nt
	v_add_co_u32_e32 v42, vcc, s2, v0
	s_mov_b32 s2, 0x4e000
	s_nop 0
	v_addc_co_u32_e32 v43, vcc, 0, v1, vcc
	v_add_co_u32_e32 v44, vcc, s2, v0
	s_mov_b32 s2, 0x4c000
	s_nop 0
	v_addc_co_u32_e32 v45, vcc, 0, v1, vcc
	global_load_dword v42, v[42:43], off nt
	s_nop 0
	global_load_dword v43, v[44:45], off nt
	v_add_co_u32_e32 v44, vcc, s2, v0
	s_mov_b32 s2, 0x4a000
	s_nop 0
	v_addc_co_u32_e32 v45, vcc, 0, v1, vcc
	v_add_co_u32_e32 v46, vcc, s2, v0
	s_mov_b32 s2, 0x48000
	s_nop 0
	v_addc_co_u32_e32 v47, vcc, 0, v1, vcc
	global_load_dword v44, v[44:45], off nt
	s_nop 0
	global_load_dword v45, v[46:47], off nt
	v_add_co_u32_e32 v46, vcc, s2, v0
	s_mov_b32 s2, 0x46000
	s_nop 0
	v_addc_co_u32_e32 v47, vcc, 0, v1, vcc
	v_add_co_u32_e32 v48, vcc, s2, v0
	s_mov_b32 s2, 0x44000
	s_nop 0
	v_addc_co_u32_e32 v49, vcc, 0, v1, vcc
	v_add_co_u32_e32 v50, vcc, s2, v0
	s_mov_b32 s2, 0x42000
	s_nop 0
	v_addc_co_u32_e32 v51, vcc, 0, v1, vcc
	v_add_co_u32_e32 v52, vcc, s2, v0
	s_mov_b32 s2, 0x40000
	s_nop 0
	v_addc_co_u32_e32 v53, vcc, 0, v1, vcc
	v_add_co_u32_e32 v54, vcc, s2, v0
	s_mov_b32 s2, 0x7e000
	s_nop 0
	v_addc_co_u32_e32 v55, vcc, 0, v1, vcc
	v_add_co_u32_e32 v56, vcc, s2, v0
	s_mov_b32 s2, 0x7c000
	s_nop 0
	v_addc_co_u32_e32 v57, vcc, 0, v1, vcc
	global_load_dword v46, v[46:47], off nt
	s_nop 0
	global_load_dword v48, v[48:49], off nt
	s_nop 0
	global_load_dword v50, v[50:51], off nt
	s_nop 0
	global_load_dword v52, v[52:53], off nt
	s_nop 0
	global_load_dword v54, v[54:55], off nt
	s_nop 0
	global_load_dword v47, v[56:57], off nt
	v_add_co_u32_e32 v56, vcc, s2, v0
	s_mov_b32 s2, 0x7a000
	s_nop 0
	v_addc_co_u32_e32 v57, vcc, 0, v1, vcc
	global_load_dword v49, v[56:57], off nt
	v_add_co_u32_e32 v56, vcc, s2, v0
	s_mov_b32 s2, 0x78000
	s_nop 0
	v_addc_co_u32_e32 v57, vcc, 0, v1, vcc
	global_load_dword v51, v[56:57], off nt
	v_add_co_u32_e32 v56, vcc, s2, v0
	s_mov_b32 s2, 0x76000
	s_nop 0
	v_addc_co_u32_e32 v57, vcc, 0, v1, vcc
	global_load_dword v53, v[56:57], off nt
	v_add_co_u32_e32 v56, vcc, s2, v0
	s_mov_b32 s2, 0x74000
	s_nop 0
	v_addc_co_u32_e32 v57, vcc, 0, v1, vcc
	global_load_dword v55, v[56:57], off nt
	v_add_co_u32_e32 v56, vcc, s2, v0
	s_mov_b32 s2, 0x72000
	s_nop 0
	v_addc_co_u32_e32 v57, vcc, 0, v1, vcc
	v_add_co_u32_e32 v58, vcc, s2, v0
	s_mov_b32 s2, 0x70000
	s_nop 0
	v_addc_co_u32_e32 v59, vcc, 0, v1, vcc
	global_load_dword v56, v[56:57], off nt
	s_nop 0
	global_load_dword v57, v[58:59], off nt
	v_add_co_u32_e32 v58, vcc, s2, v0
	s_mov_b32 s2, 0x6e000
	s_nop 0
	v_addc_co_u32_e32 v59, vcc, 0, v1, vcc
	v_add_co_u32_e32 v60, vcc, s2, v0
	s_mov_b32 s2, 0x6c000
	s_nop 0
	v_addc_co_u32_e32 v61, vcc, 0, v1, vcc
	global_load_dword v58, v[58:59], off nt
	s_nop 0
	global_load_dword v59, v[60:61], off nt
	v_add_co_u32_e32 v60, vcc, s2, v0
	s_mov_b32 s2, 0x6a000
	s_nop 0
	v_addc_co_u32_e32 v61, vcc, 0, v1, vcc
	v_add_co_u32_e32 v62, vcc, s2, v0
	s_mov_b32 s2, 0x68000
	s_nop 0
	v_addc_co_u32_e32 v63, vcc, 0, v1, vcc
	global_load_dword v60, v[60:61], off nt
	s_nop 0
	global_load_dword v61, v[62:63], off nt
	v_add_co_u32_e32 v62, vcc, s2, v0
	s_mov_b32 s2, 0x66000
	s_nop 0
	v_addc_co_u32_e32 v63, vcc, 0, v1, vcc
	v_add_co_u32_e32 v64, vcc, s2, v0
	s_mov_b32 s2, 0x64000
	s_nop 0
	v_addc_co_u32_e32 v65, vcc, 0, v1, vcc
	v_add_co_u32_e32 v66, vcc, s2, v0
	s_mov_b32 s2, 0x62000
	s_nop 0
	v_addc_co_u32_e32 v67, vcc, 0, v1, vcc
	v_add_co_u32_e32 v68, vcc, s2, v0
	s_mov_b32 s2, 0x60000
	s_nop 0
	v_addc_co_u32_e32 v69, vcc, 0, v1, vcc
	v_add_co_u32_e32 v70, vcc, s2, v0
	s_mov_b32 s2, 0x9e000
	s_nop 0
	v_addc_co_u32_e32 v71, vcc, 0, v1, vcc
	v_add_co_u32_e32 v72, vcc, s2, v0
	s_mov_b32 s2, 0x9c000
	s_nop 0
	v_addc_co_u32_e32 v73, vcc, 0, v1, vcc
	global_load_dword v62, v[62:63], off nt
	s_nop 0
	global_load_dword v64, v[64:65], off nt
	s_nop 0
	global_load_dword v66, v[66:67], off nt
	s_nop 0
	global_load_dword v68, v[68:69], off nt
	s_nop 0
	global_load_dword v70, v[70:71], off nt
	s_nop 0
	global_load_dword v63, v[72:73], off nt
	v_add_co_u32_e32 v72, vcc, s2, v0
	s_mov_b32 s2, 0x9a000
	s_nop 0
	v_addc_co_u32_e32 v73, vcc, 0, v1, vcc
	global_load_dword v65, v[72:73], off nt
	v_add_co_u32_e32 v72, vcc, s2, v0
	s_mov_b32 s2, 0x98000
	s_nop 0
	v_addc_co_u32_e32 v73, vcc, 0, v1, vcc
	global_load_dword v67, v[72:73], off nt
	v_add_co_u32_e32 v72, vcc, s2, v0
	s_mov_b32 s2, 0x96000
	s_nop 0
	v_addc_co_u32_e32 v73, vcc, 0, v1, vcc
	global_load_dword v69, v[72:73], off nt
	v_add_co_u32_e32 v72, vcc, s2, v0
	s_mov_b32 s2, 0x94000
	s_nop 0
	v_addc_co_u32_e32 v73, vcc, 0, v1, vcc
	global_load_dword v71, v[72:73], off nt
	v_add_co_u32_e32 v72, vcc, s2, v0
	s_mov_b32 s2, 0x92000
	s_nop 0
	v_addc_co_u32_e32 v73, vcc, 0, v1, vcc
	v_add_co_u32_e32 v74, vcc, s2, v0
	s_mov_b32 s2, 0x90000
	s_nop 0
	v_addc_co_u32_e32 v75, vcc, 0, v1, vcc
	global_load_dword v72, v[72:73], off nt
	s_nop 0
	global_load_dword v73, v[74:75], off nt
	v_add_co_u32_e32 v74, vcc, s2, v0
	s_mov_b32 s2, 0x8e000
	s_nop 0
	v_addc_co_u32_e32 v75, vcc, 0, v1, vcc
	v_add_co_u32_e32 v76, vcc, s2, v0
	s_mov_b32 s2, 0x8c000
	s_nop 0
	v_addc_co_u32_e32 v77, vcc, 0, v1, vcc
	global_load_dword v74, v[74:75], off nt
	s_nop 0
	global_load_dword v75, v[76:77], off nt
	v_add_co_u32_e32 v76, vcc, s2, v0
	s_mov_b32 s2, 0x8a000
	s_nop 0
	v_addc_co_u32_e32 v77, vcc, 0, v1, vcc
	v_add_co_u32_e32 v78, vcc, s2, v0
	s_mov_b32 s2, 0x88000
	s_nop 0
	v_addc_co_u32_e32 v79, vcc, 0, v1, vcc
	global_load_dword v76, v[76:77], off nt
	s_nop 0
	global_load_dword v77, v[78:79], off nt
	v_add_co_u32_e32 v78, vcc, s2, v0
	s_mov_b32 s2, 0x86000
	s_nop 0
	v_addc_co_u32_e32 v79, vcc, 0, v1, vcc
	v_add_co_u32_e32 v80, vcc, s2, v0
	s_mov_b32 s2, 0x84000
	s_nop 0
	v_addc_co_u32_e32 v81, vcc, 0, v1, vcc
	v_add_co_u32_e32 v82, vcc, s2, v0
	s_mov_b32 s2, 0x82000
	s_nop 0
	v_addc_co_u32_e32 v83, vcc, 0, v1, vcc
	v_add_co_u32_e32 v84, vcc, s2, v0
	s_mov_b32 s2, 0x80000
	s_nop 0
	v_addc_co_u32_e32 v85, vcc, 0, v1, vcc
	v_add_co_u32_e32 v86, vcc, s2, v0
	s_mov_b32 s2, 0xbe000
	s_nop 0
	v_addc_co_u32_e32 v87, vcc, 0, v1, vcc
	v_add_co_u32_e32 v88, vcc, s2, v0
	s_mov_b32 s2, 0xbc000
	s_nop 0
	v_addc_co_u32_e32 v89, vcc, 0, v1, vcc
	global_load_dword v78, v[78:79], off nt
	s_nop 0
	global_load_dword v80, v[80:81], off nt
	s_nop 0
	global_load_dword v82, v[82:83], off nt
	s_nop 0
	global_load_dword v84, v[84:85], off nt
	s_nop 0
	global_load_dword v86, v[86:87], off nt
	s_nop 0
	global_load_dword v79, v[88:89], off nt
	v_add_co_u32_e32 v88, vcc, s2, v0
	s_mov_b32 s2, 0xba000
	s_nop 0
	v_addc_co_u32_e32 v89, vcc, 0, v1, vcc
	global_load_dword v81, v[88:89], off nt
	v_add_co_u32_e32 v88, vcc, s2, v0
	s_mov_b32 s2, 0xb8000
	s_nop 0
	v_addc_co_u32_e32 v89, vcc, 0, v1, vcc
	global_load_dword v83, v[88:89], off nt
	v_add_co_u32_e32 v88, vcc, s2, v0
	s_mov_b32 s2, 0xb6000
	s_nop 0
	v_addc_co_u32_e32 v89, vcc, 0, v1, vcc
	global_load_dword v85, v[88:89], off nt
	v_add_co_u32_e32 v88, vcc, s2, v0
	s_mov_b32 s2, 0xb4000
	s_nop 0
	v_addc_co_u32_e32 v89, vcc, 0, v1, vcc
	global_load_dword v87, v[88:89], off nt
	v_add_co_u32_e32 v88, vcc, s2, v0
	s_mov_b32 s2, 0xb2000
	s_nop 0
	v_addc_co_u32_e32 v89, vcc, 0, v1, vcc
	v_add_co_u32_e32 v90, vcc, s2, v0
	s_mov_b32 s2, 0xb0000
	s_nop 0
	v_addc_co_u32_e32 v91, vcc, 0, v1, vcc
	global_load_dword v88, v[88:89], off nt
	s_nop 0
	global_load_dword v89, v[90:91], off nt
	v_add_co_u32_e32 v90, vcc, s2, v0
	s_mov_b32 s2, 0xae000
	s_nop 0
	v_addc_co_u32_e32 v91, vcc, 0, v1, vcc
	v_add_co_u32_e32 v92, vcc, s2, v0
	s_mov_b32 s2, 0xac000
	s_nop 0
	v_addc_co_u32_e32 v93, vcc, 0, v1, vcc
	global_load_dword v90, v[90:91], off nt
	s_nop 0
	global_load_dword v91, v[92:93], off nt
	v_add_co_u32_e32 v92, vcc, s2, v0
	s_mov_b32 s2, 0xaa000
	s_nop 0
	v_addc_co_u32_e32 v93, vcc, 0, v1, vcc
	v_add_co_u32_e32 v94, vcc, s2, v0
	s_mov_b32 s2, 0xa8000
	s_nop 0
	v_addc_co_u32_e32 v95, vcc, 0, v1, vcc
	global_load_dword v92, v[92:93], off nt
	s_nop 0
	global_load_dword v93, v[94:95], off nt
	v_add_co_u32_e32 v94, vcc, s2, v0
	s_mov_b32 s2, 0xa6000
	s_nop 0
	v_addc_co_u32_e32 v95, vcc, 0, v1, vcc
	v_add_co_u32_e32 v98, vcc, s2, v0
	s_mov_b32 s2, 0xa4000
	s_nop 0
	v_addc_co_u32_e32 v99, vcc, 0, v1, vcc
	global_load_dword v94, v[94:95], off nt
	s_nop 0
	global_load_dword v138, v[98:99], off nt
	v_add_co_u32_e32 v98, vcc, s2, v0
	s_mov_b32 s2, 0xa2000
	s_nop 0
	v_addc_co_u32_e32 v99, vcc, 0, v1, vcc
	global_load_dword v104, v[98:99], off nt
	v_add_co_u32_e32 v98, vcc, s2, v0
	s_mov_b32 s2, 0xa0000
	s_nop 0
	v_addc_co_u32_e32 v99, vcc, 0, v1, vcc
	global_load_dword v105, v[98:99], off nt
	v_add_co_u32_e32 v98, vcc, s2, v0
	s_mov_b32 s2, 0xde000
	s_nop 0
	v_addc_co_u32_e32 v99, vcc, 0, v1, vcc
	global_load_dword v106, v[98:99], off nt
	v_add_co_u32_e32 v98, vcc, s2, v0
	s_mov_b32 s2, 0xdc000
	s_nop 0
	v_addc_co_u32_e32 v99, vcc, 0, v1, vcc
	global_load_dword v95, v[98:99], off nt
	v_add_co_u32_e32 v98, vcc, s2, v0
	s_mov_b32 s2, 0xda000
	s_nop 0
	v_addc_co_u32_e32 v99, vcc, 0, v1, vcc
	v_add_co_u32_e32 v100, vcc, s2, v0
	s_mov_b32 s2, 0xd8000
	s_nop 0
	v_addc_co_u32_e32 v101, vcc, 0, v1, vcc
	global_load_dword v98, v[98:99], off nt
	s_nop 0
	global_load_dword v99, v[100:101], off nt
	v_add_co_u32_e32 v100, vcc, s2, v0
	s_mov_b32 s2, 0xd6000
	s_nop 0
	v_addc_co_u32_e32 v101, vcc, 0, v1, vcc
	global_load_dword v107, v[100:101], off nt
	v_add_co_u32_e32 v100, vcc, s2, v0
	s_mov_b32 s2, 0xd4000
	s_nop 0
	v_addc_co_u32_e32 v101, vcc, 0, v1, vcc
	global_load_dword v108, v[100:101], off nt
	v_add_co_u32_e32 v100, vcc, s2, v0
	s_mov_b32 s2, 0xd2000
	s_nop 0
	v_addc_co_u32_e32 v101, vcc, 0, v1, vcc
	global_load_dword v109, v[100:101], off nt
	v_add_co_u32_e32 v100, vcc, s2, v0
	s_mov_b32 s2, 0xd0000
	s_nop 0
	v_addc_co_u32_e32 v101, vcc, 0, v1, vcc
	global_load_dword v110, v[100:101], off nt
	v_add_co_u32_e32 v100, vcc, s2, v0
	s_mov_b32 s2, 0xce000
	s_nop 0
	v_addc_co_u32_e32 v101, vcc, 0, v1, vcc
	global_load_dword v111, v[100:101], off nt
	v_add_co_u32_e32 v100, vcc, s2, v0
	s_mov_b32 s2, 0xcc000
	s_nop 0
	v_addc_co_u32_e32 v101, vcc, 0, v1, vcc
	global_load_dword v112, v[100:101], off nt
	v_add_co_u32_e32 v100, vcc, s2, v0
	s_mov_b32 s2, 0xca000
	s_nop 0
	v_addc_co_u32_e32 v101, vcc, 0, v1, vcc
	global_load_dword v113, v[100:101], off nt
	v_add_co_u32_e32 v100, vcc, s2, v0
	s_mov_b32 s2, 0xc8000
	s_nop 0
	v_addc_co_u32_e32 v101, vcc, 0, v1, vcc
	global_load_dword v114, v[100:101], off nt
	v_add_co_u32_e32 v100, vcc, s2, v0
	s_mov_b32 s2, 0xc6000
	s_nop 0
	v_addc_co_u32_e32 v101, vcc, 0, v1, vcc
	global_load_dword v115, v[100:101], off nt
	v_add_co_u32_e32 v100, vcc, s2, v0
	s_mov_b32 s2, 0xc4000
	s_nop 0
	v_addc_co_u32_e32 v101, vcc, 0, v1, vcc
	global_load_dword v116, v[100:101], off nt
	v_add_co_u32_e32 v100, vcc, s2, v0
	s_mov_b32 s2, 0xc2000
	s_nop 0
	v_addc_co_u32_e32 v101, vcc, 0, v1, vcc
	global_load_dword v117, v[100:101], off nt
	v_add_co_u32_e32 v100, vcc, s2, v0
	s_mov_b32 s2, 0xc0000
	s_nop 0
	v_addc_co_u32_e32 v101, vcc, 0, v1, vcc
	global_load_dword v118, v[100:101], off nt
	v_add_co_u32_e32 v100, vcc, s2, v0
	s_mov_b32 s2, 0xfe000
	s_nop 0
	v_addc_co_u32_e32 v101, vcc, 0, v1, vcc
	global_load_dword v119, v[100:101], off nt
	v_add_co_u32_e32 v100, vcc, s2, v0
	s_mov_b32 s2, 0xfc000
	s_nop 0
	v_addc_co_u32_e32 v101, vcc, 0, v1, vcc
	global_load_dword v120, v[100:101], off nt
	v_add_co_u32_e32 v100, vcc, s2, v0
	s_mov_b32 s2, 0xfa000
	s_nop 0
	v_addc_co_u32_e32 v101, vcc, 0, v1, vcc
	global_load_dword v121, v[100:101], off nt
	v_add_co_u32_e32 v100, vcc, s2, v0
	s_mov_b32 s2, 0xf8000
	s_nop 0
	v_addc_co_u32_e32 v101, vcc, 0, v1, vcc
	global_load_dword v122, v[100:101], off nt
	v_add_co_u32_e32 v100, vcc, s2, v0
	s_mov_b32 s2, 0xf6000
	s_nop 0
	v_addc_co_u32_e32 v101, vcc, 0, v1, vcc
	global_load_dword v123, v[100:101], off nt
	v_add_co_u32_e32 v100, vcc, s2, v0
	s_mov_b32 s2, 0xf4000
	s_nop 0
	v_addc_co_u32_e32 v101, vcc, 0, v1, vcc
	global_load_dword v124, v[100:101], off nt
	v_add_co_u32_e32 v100, vcc, s2, v0
	s_mov_b32 s2, 0xf2000
	s_nop 0
	v_addc_co_u32_e32 v101, vcc, 0, v1, vcc
	global_load_dword v125, v[100:101], off nt
	v_add_co_u32_e32 v100, vcc, s2, v0
	s_mov_b32 s2, 0xf0000
	s_nop 0
	v_addc_co_u32_e32 v101, vcc, 0, v1, vcc
	global_load_dword v126, v[100:101], off nt
	v_add_co_u32_e32 v100, vcc, s2, v0
	s_mov_b32 s2, 0xee000
	s_nop 0
	v_addc_co_u32_e32 v101, vcc, 0, v1, vcc
	global_load_dword v127, v[100:101], off nt
	v_add_co_u32_e32 v100, vcc, s2, v0
	s_mov_b32 s2, 0xec000
	s_nop 0
	v_addc_co_u32_e32 v101, vcc, 0, v1, vcc
	global_load_dword v128, v[100:101], off nt
	v_add_co_u32_e32 v100, vcc, s2, v0
	s_mov_b32 s2, 0xea000
	s_nop 0
	v_addc_co_u32_e32 v101, vcc, 0, v1, vcc
	global_load_dword v129, v[100:101], off nt
	v_add_co_u32_e32 v100, vcc, s2, v0
	s_mov_b32 s2, 0xe8000
	s_nop 0
	v_addc_co_u32_e32 v101, vcc, 0, v1, vcc
	global_load_dword v130, v[100:101], off nt
	v_add_co_u32_e32 v100, vcc, s2, v0
	s_mov_b32 s2, 0xe6000
	s_nop 0
	v_addc_co_u32_e32 v101, vcc, 0, v1, vcc
	global_load_dword v131, v[100:101], off nt
	v_add_co_u32_e32 v100, vcc, s2, v0
	s_mov_b32 s2, 0xe4000
	s_nop 0
	v_addc_co_u32_e32 v101, vcc, 0, v1, vcc
	global_load_dword v132, v[100:101], off nt
	v_add_co_u32_e32 v100, vcc, s2, v0
	s_mov_b32 s2, 0xe2000
	s_nop 0
	v_addc_co_u32_e32 v101, vcc, 0, v1, vcc
	global_load_dword v133, v[100:101], off nt
	v_add_co_u32_e32 v100, vcc, s2, v0
	s_mov_b32 s2, 0xe0000
	s_nop 0
	v_addc_co_u32_e32 v101, vcc, 0, v1, vcc
	v_add_co_u32_e32 v0, vcc, s2, v0
	global_load_dword v134, v[100:101], off nt
	s_nop 0
	v_addc_co_u32_e32 v1, vcc, 0, v1, vcc
	global_load_dword v135, v[0:1], off nt
	v_mov_b32_e32 v0, s18
	s_movk_i32 s2, 0x90
	s_waitcnt vmcnt(62)
	v_mad_u32_u24 v136, v6, s2, v0
	v_mul_f32_e32 v0, 0x42000000, v22
	v_mul_f32_e32 v1, 0x42000000, v21
	v_mov_b32_e32 v100, v97
	v_cvt_pk_fp8_f32 v100, v0, v1
	v_mul_f32_e32 v0, 0x42000000, v15
	v_mul_f32_e32 v1, 0x42000000, v13
	v_mov_b32_e32 v101, v97
	v_cvt_pk_fp8_f32 v101, v0, v1
	v_mul_f32_e32 v0, 0x42000000, v10
	v_mul_f32_e32 v1, 0x42000000, v9
	v_cvt_pk_fp8_f32 v102, v0, v1
	v_mul_f32_e32 v0, 0x42000000, v5
	v_mul_f32_e32 v1, 0x42000000, v4
	v_cvt_pk_fp8_f32 v103, v0, v1
	v_mul_f32_e32 v3, 0x42000000, v3
	v_mul_f32_e32 v2, 0x42000000, v2
	v_cvt_pk_fp8_f32 v103, v3, v2 op_sel:[0,0,1]
	v_mul_f32_e32 v1, 0x42000000, v38
	v_mul_f32_e32 v2, 0x42000000, v36
	v_mov_b32_e32 v0, v97
	v_cvt_pk_fp8_f32 v0, v1, v2
	v_mul_f32_e32 v3, 0x42000000, v34
	v_mul_f32_e32 v4, 0x42000000, v32
	v_mul_f32_e32 v2, 0x42000000, v30
	v_cvt_pk_fp8_f32 v0, v3, v4 op_sel:[0,0,1]
	v_mul_f32_e32 v3, 0x42000000, v29
	v_mov_b32_e32 v1, v97
	v_cvt_pk_fp8_f32 v1, v2, v3
	v_mul_f32_e32 v4, 0x42000000, v28
	v_mul_f32_e32 v5, 0x42000000, v27
	v_mul_f32_e32 v3, 0x42000000, v26
	v_cvt_pk_fp8_f32 v1, v4, v5 op_sel:[0,0,1]
	v_mul_f32_e32 v4, 0x42000000, v25
	v_mov_b32_e32 v2, v97
	v_cvt_pk_fp8_f32 v2, v3, v4
	v_mul_f32_e32 v8, 0x42000000, v8
	v_mul_f32_e32 v7, 0x42000000, v7
	v_cvt_pk_fp8_f32 v102, v8, v7 op_sel:[0,0,1]
	v_mul_f32_e32 v5, 0x42000000, v24
	v_mul_f32_e32 v7, 0x42000000, v23
	v_cvt_pk_fp8_f32 v2, v5, v7 op_sel:[0,0,1]
	v_mul_f32_e32 v4, 0x42000000, v20
	v_mul_f32_e32 v5, 0x42000000, v18
	v_mov_b32_e32 v3, v97
	v_cvt_pk_fp8_f32 v3, v4, v5
	v_mul_f32_e32 v7, 0x42000000, v16
	v_mul_f32_e32 v8, 0x42000000, v14
	v_cvt_pk_fp8_f32 v3, v7, v8 op_sel:[0,0,1]
	s_waitcnt vmcnt(48)
	s_waitcnt vmcnt(32)
	s_waitcnt vmcnt(16)
	s_waitcnt vmcnt(0)
	ds_write_b128 v136, v[0:3] offset:16
	v_mul_f32_e32 v1, 0x42000000, v54
	v_mul_f32_e32 v2, 0x42000000, v52
	v_mov_b32_e32 v0, v97
	v_cvt_pk_fp8_f32 v0, v1, v2
	v_mul_f32_e32 v3, 0x42000000, v50
	v_mul_f32_e32 v4, 0x42000000, v48
	v_mul_f32_e32 v2, 0x42000000, v46
	v_cvt_pk_fp8_f32 v0, v3, v4 op_sel:[0,0,1]
	v_mul_f32_e32 v3, 0x42000000, v45
	v_mov_b32_e32 v1, v97
	v_cvt_pk_fp8_f32 v1, v2, v3
	v_mul_f32_e32 v4, 0x42000000, v44
	v_mul_f32_e32 v5, 0x42000000, v43
	v_mul_f32_e32 v3, 0x42000000, v42
	v_cvt_pk_fp8_f32 v1, v4, v5 op_sel:[0,0,1]
	v_mul_f32_e32 v4, 0x42000000, v41
	v_mov_b32_e32 v2, v97
	v_cvt_pk_fp8_f32 v2, v3, v4
	v_mul_f32_e32 v5, 0x42000000, v40
	v_mul_f32_e32 v7, 0x42000000, v39
	v_mul_f32_e32 v4, 0x42000000, v37
	v_cvt_pk_fp8_f32 v2, v5, v7 op_sel:[0,0,1]
	v_mul_f32_e32 v5, 0x42000000, v35
	v_mov_b32_e32 v3, v97
	v_cvt_pk_fp8_f32 v3, v4, v5
	v_mul_f32_e32 v7, 0x42000000, v33
	v_mul_f32_e32 v8, 0x42000000, v31
	v_mul_f32_e32 v4, 0x42000000, v64
	v_cvt_pk_fp8_f32 v3, v7, v8 op_sel:[0,0,1]
	v_mul_f32_e32 v5, 0x42000000, v59
	v_mul_f32_e32 v7, 0x42000000, v55
	v_mul_f32_e32 v8, 0x42000000, v47
	ds_write_b128 v136, v[0:3] offset:32
	v_mul_f32_e32 v1, 0x42000000, v70
	v_mul_f32_e32 v2, 0x42000000, v68
	v_mov_b32_e32 v0, v97
	v_cvt_pk_fp8_f32 v0, v1, v2
	v_mul_f32_e32 v3, 0x42000000, v66
	v_mul_f32_e32 v2, 0x42000000, v62
	v_mov_b32_e32 v1, v97
	v_cvt_pk_fp8_f32 v0, v3, v4 op_sel:[0,0,1]
	v_mul_f32_e32 v3, 0x42000000, v61
	v_cvt_pk_fp8_f32 v1, v2, v3
	v_mul_f32_e32 v4, 0x42000000, v60
	v_mul_f32_e32 v3, 0x42000000, v58
	v_mov_b32_e32 v2, v97
	v_cvt_pk_fp8_f32 v1, v4, v5 op_sel:[0,0,1]
	v_mul_f32_e32 v4, 0x42000000, v57
	v_cvt_pk_fp8_f32 v2, v3, v4
	v_mul_f32_e32 v5, 0x42000000, v56
	v_mul_f32_e32 v4, 0x42000000, v53
	v_mov_b32_e32 v3, v97
	v_cvt_pk_fp8_f32 v2, v5, v7 op_sel:[0,0,1]
	v_mul_f32_e32 v5, 0x42000000, v51
	v_cvt_pk_fp8_f32 v3, v4, v5
	v_mul_f32_e32 v7, 0x42000000, v49
	v_mul_f32_e32 v4, 0x42000000, v80
	v_mul_f32_e32 v5, 0x42000000, v75
	v_cvt_pk_fp8_f32 v3, v7, v8 op_sel:[0,0,1]
	v_mul_f32_e32 v7, 0x42000000, v71
	v_mul_f32_e32 v8, 0x42000000, v63
	v_mul_f32_e32 v19, 0x42000000, v19
	ds_write_b128 v136, v[0:3] offset:48
	v_mul_f32_e32 v1, 0x42000000, v86
	v_mul_f32_e32 v2, 0x42000000, v84
	v_mov_b32_e32 v0, v97
	v_cvt_pk_fp8_f32 v0, v1, v2
	v_mul_f32_e32 v3, 0x42000000, v82
	v_mul_f32_e32 v2, 0x42000000, v78
	v_mov_b32_e32 v1, v97
	v_cvt_pk_fp8_f32 v0, v3, v4 op_sel:[0,0,1]
	v_mul_f32_e32 v3, 0x42000000, v77
	v_cvt_pk_fp8_f32 v1, v2, v3
	v_mul_f32_e32 v4, 0x42000000, v76
	v_mul_f32_e32 v3, 0x42000000, v74
	v_mov_b32_e32 v2, v97
	v_cvt_pk_fp8_f32 v1, v4, v5 op_sel:[0,0,1]
	v_mul_f32_e32 v4, 0x42000000, v73
	v_cvt_pk_fp8_f32 v2, v3, v4
	v_mul_f32_e32 v5, 0x42000000, v72
	v_mul_f32_e32 v4, 0x42000000, v69
	v_mov_b32_e32 v3, v97
	v_cvt_pk_fp8_f32 v2, v5, v7 op_sel:[0,0,1]
	v_mul_f32_e32 v5, 0x42000000, v67
	v_cvt_pk_fp8_f32 v3, v4, v5
	v_mul_f32_e32 v7, 0x42000000, v65
	v_mul_f32_e32 v4, 0x42000000, v138
	v_mul_f32_e32 v5, 0x42000000, v91
	v_cvt_pk_fp8_f32 v3, v7, v8 op_sel:[0,0,1]
	v_mul_f32_e32 v7, 0x42000000, v87
	v_mul_f32_e32 v8, 0x42000000, v79
	v_mul_f32_e32 v17, 0x42000000, v17
	ds_write_b128 v136, v[0:3] offset:64
	v_mul_f32_e32 v1, 0x42000000, v106
	v_mul_f32_e32 v2, 0x42000000, v105
	v_mov_b32_e32 v0, v97
	v_cvt_pk_fp8_f32 v0, v1, v2
	v_mul_f32_e32 v3, 0x42000000, v104
	v_mul_f32_e32 v2, 0x42000000, v94
	v_mov_b32_e32 v1, v97
	v_cvt_pk_fp8_f32 v0, v3, v4 op_sel:[0,0,1]
	v_mul_f32_e32 v3, 0x42000000, v93
	v_cvt_pk_fp8_f32 v1, v2, v3
	v_mul_f32_e32 v4, 0x42000000, v92
	v_mul_f32_e32 v3, 0x42000000, v90
	v_mov_b32_e32 v2, v97
	v_cvt_pk_fp8_f32 v1, v4, v5 op_sel:[0,0,1]
	v_mul_f32_e32 v4, 0x42000000, v89
	v_cvt_pk_fp8_f32 v2, v3, v4
	v_mul_f32_e32 v5, 0x42000000, v88
	v_mul_f32_e32 v4, 0x42000000, v85
	v_mov_b32_e32 v3, v97
	v_cvt_pk_fp8_f32 v2, v5, v7 op_sel:[0,0,1]
	v_mul_f32_e32 v5, 0x42000000, v83
	v_cvt_pk_fp8_f32 v3, v4, v5
	v_mul_f32_e32 v7, 0x42000000, v81
	v_mul_f32_e32 v4, 0x42000000, v116
	v_mul_f32_e32 v5, 0x42000000, v112
	v_cvt_pk_fp8_f32 v3, v7, v8 op_sel:[0,0,1]
	v_mul_f32_e32 v7, 0x42000000, v108
	v_mul_f32_e32 v8, 0x42000000, v95
	v_mul_f32_e32 v12, 0x42000000, v12
	ds_write_b128 v136, v[0:3] offset:80
	v_mul_f32_e32 v1, 0x42000000, v119
	v_mul_f32_e32 v2, 0x42000000, v118
	v_mov_b32_e32 v0, v97
	v_cvt_pk_fp8_f32 v0, v1, v2
	v_mul_f32_e32 v3, 0x42000000, v117
	v_mul_f32_e32 v2, 0x42000000, v115
	v_mov_b32_e32 v1, v97
	v_cvt_pk_fp8_f32 v0, v3, v4 op_sel:[0,0,1]
	v_mul_f32_e32 v3, 0x42000000, v114
	v_cvt_pk_fp8_f32 v1, v2, v3
	v_mul_f32_e32 v4, 0x42000000, v113
	v_mul_f32_e32 v3, 0x42000000, v111
	v_mov_b32_e32 v2, v97
	v_cvt_pk_fp8_f32 v1, v4, v5 op_sel:[0,0,1]
	v_mul_f32_e32 v4, 0x42000000, v110
	v_cvt_pk_fp8_f32 v2, v3, v4
	v_mul_f32_e32 v5, 0x42000000, v109
	v_mul_f32_e32 v4, 0x42000000, v107
	v_mov_b32_e32 v3, v97
	v_cvt_pk_fp8_f32 v2, v5, v7 op_sel:[0,0,1]
	v_mul_f32_e32 v5, 0x42000000, v99
	v_cvt_pk_fp8_f32 v3, v4, v5
	v_mul_f32_e32 v7, 0x42000000, v98
	v_mul_f32_e32 v4, 0x42000000, v132
	v_mul_f32_e32 v5, 0x42000000, v128
	v_cvt_pk_fp8_f32 v3, v7, v8 op_sel:[0,0,1]
	v_mul_f32_e32 v7, 0x42000000, v124
	v_mul_f32_e32 v8, 0x42000000, v120
	v_mul_f32_e32 v11, 0x42000000, v11
	ds_write_b128 v136, v[0:3] offset:96
	v_mul_f32_e32 v1, 0x42000000, v135
	v_mul_f32_e32 v2, 0x42000000, v134
	v_mov_b32_e32 v0, v97
	v_cvt_pk_fp8_f32 v0, v1, v2
	v_mul_f32_e32 v3, 0x42000000, v133
	v_mul_f32_e32 v2, 0x42000000, v131
	v_mov_b32_e32 v1, v97
	v_cvt_pk_fp8_f32 v0, v3, v4 op_sel:[0,0,1]
	v_mul_f32_e32 v3, 0x42000000, v130
	v_cvt_pk_fp8_f32 v1, v2, v3
	v_mul_f32_e32 v4, 0x42000000, v129
	v_mul_f32_e32 v3, 0x42000000, v127
	v_mov_b32_e32 v2, v97
	v_cvt_pk_fp8_f32 v1, v4, v5 op_sel:[0,0,1]
	v_mul_f32_e32 v4, 0x42000000, v126
	v_cvt_pk_fp8_f32 v2, v3, v4
	v_mul_f32_e32 v5, 0x42000000, v125
	v_mul_f32_e32 v4, 0x42000000, v123
	v_mov_b32_e32 v3, v97
	v_cvt_pk_fp8_f32 v2, v5, v7 op_sel:[0,0,1]
	v_mul_f32_e32 v5, 0x42000000, v122
	v_cvt_pk_fp8_f32 v3, v4, v5
	v_mul_f32_e32 v7, 0x42000000, v121
	v_cvt_pk_fp8_f32 v100, v19, v17 op_sel:[0,0,1]
	v_cvt_pk_fp8_f32 v101, v12, v11 op_sel:[0,0,1]
	v_cvt_pk_fp8_f32 v3, v7, v8 op_sel:[0,0,1]
	v_lshrrev_b32_e32 v8, 3, v6
	s_and_b32 s2, s24, 0x700
	ds_write_b128 v136, v[100:103]
	ds_write_b128 v136, v[0:3] offset:112
	v_lshlrev_b32_e32 v0, 4, v6
	v_and_b32_e32 v138, 0x70, v0
	v_and_b32_e32 v0, 0x80, v0
	v_or_b32_e32 v6, s2, v0
	v_mul_u32_u24_e32 v0, 0x90, v8
	s_waitcnt lgkmcnt(0)
	s_add_u32 s2, s21, s23
	v_add3_u32 v7, s18, v138, v0
	s_addc_u32 s3, s22, 0
	ds_read_b128 v[0:3], v7
	v_or_b32_e32 v8, s20, v8
	v_lshl_add_u64 v[4:5], s[2:3], 0, v[138:139]
	v_lshrrev_b32_e32 v9, 1, v8
	s_movk_i32 s2, 0x63
	v_and_or_b32 v9, v9, s2, v6
	v_lshlrev_b32_e32 v138, 10, v9
	v_lshl_add_u64 v[10:11], v[4:5], 0, v[138:139]
	s_waitcnt lgkmcnt(0)
	global_store_dwordx4 v[10:11], v[0:3], off
	ds_read_b128 v[0:3], v7 offset:1152
	v_or_b32_e32 v9, 8, v8
	v_lshrrev_b32_e32 v9, 1, v9
	s_movk_i32 s2, 0x67
	v_and_or_b32 v9, v9, s2, v6
	v_lshlrev_b32_e32 v138, 10, v9
	v_lshl_add_u64 v[10:11], v[4:5], 0, v[138:139]
	s_waitcnt lgkmcnt(0)
	global_store_dwordx4 v[10:11], v[0:3], off
	ds_read_b128 v[0:3], v7 offset:2304
	v_or_b32_e32 v9, 16, v8
	v_lshrrev_b32_e32 v9, 1, v9
	s_movk_i32 s2, 0x6b
	v_and_or_b32 v9, v9, s2, v6
	v_lshlrev_b32_e32 v138, 10, v9
	v_lshl_add_u64 v[10:11], v[4:5], 0, v[138:139]
	s_waitcnt lgkmcnt(0)
	global_store_dwordx4 v[10:11], v[0:3], off
	ds_read_b128 v[0:3], v7 offset:3456
	v_or_b32_e32 v9, 24, v8
	v_lshrrev_b32_e32 v9, 1, v9
	s_movk_i32 s2, 0x6f
	v_and_or_b32 v9, v9, s2, v6
	v_lshlrev_b32_e32 v138, 10, v9
	v_lshl_add_u64 v[10:11], v[4:5], 0, v[138:139]
	s_waitcnt lgkmcnt(0)
	global_store_dwordx4 v[10:11], v[0:3], off
	ds_read_b128 v[0:3], v7 offset:4608
	v_or_b32_e32 v9, 32, v8
	v_lshrrev_b32_e32 v9, 1, v9
	s_movk_i32 s2, 0x73
	v_and_or_b32 v9, v9, s2, v6
	v_lshlrev_b32_e32 v138, 10, v9
	v_lshl_add_u64 v[10:11], v[4:5], 0, v[138:139]
	s_waitcnt lgkmcnt(0)
	global_store_dwordx4 v[10:11], v[0:3], off
	ds_read_b128 v[0:3], v7 offset:5760
	v_or_b32_e32 v9, 40, v8
	v_lshrrev_b32_e32 v9, 1, v9
	s_movk_i32 s2, 0x77
	v_and_or_b32 v9, v9, s2, v6
	v_lshlrev_b32_e32 v138, 10, v9
	v_lshl_add_u64 v[10:11], v[4:5], 0, v[138:139]
	s_waitcnt lgkmcnt(0)
	global_store_dwordx4 v[10:11], v[0:3], off
	ds_read_b128 v[0:3], v7 offset:6912
	v_or_b32_e32 v9, 48, v8
	v_lshrrev_b32_e32 v9, 1, v9
	s_movk_i32 s2, 0x7b
	v_and_or_b32 v9, v9, s2, v6
	v_lshlrev_b32_e32 v138, 10, v9
	v_lshl_add_u64 v[10:11], v[4:5], 0, v[138:139]
	s_waitcnt lgkmcnt(0)
	global_store_dwordx4 v[10:11], v[0:3], off
	ds_read_b128 v[0:3], v7 offset:8064
	v_or_b32_e32 v7, 56, v8
	v_lshrrev_b32_e32 v7, 1, v7
	s_movk_i32 s2, 0x7f
	v_and_or_b32 v6, v7, s2, v6
	v_lshlrev_b32_e32 v138, 10, v6
	v_lshl_add_u64 v[4:5], v[4:5], 0, v[138:139]
	s_waitcnt lgkmcnt(0)
	global_store_dwordx4 v[4:5], v[0:3], off
	s_waitcnt lgkmcnt(0)
.Lc3_done:
	s_branch .LBB0_869

	.amdhsa_kernel _Z6mk_fwd4Args
		.amdhsa_group_segment_fixed_size 0
		.amdhsa_private_segment_fixed_size 0
		.amdhsa_kernarg_size 424
		.amdhsa_user_sgpr_count 2
		.amdhsa_user_sgpr_dispatch_ptr 0
		.amdhsa_user_sgpr_queue_ptr 0
		.amdhsa_user_sgpr_kernarg_segment_ptr 1
		.amdhsa_user_sgpr_dispatch_id 0
		.amdhsa_user_sgpr_kernarg_preload_length 0
		.amdhsa_user_sgpr_kernarg_preload_offset 0
		.amdhsa_user_sgpr_private_segment_size 0
		.amdhsa_uses_dynamic_stack 0
		.amdhsa_enable_private_segment 0
		.amdhsa_system_sgpr_workgroup_id_x 1
		.amdhsa_system_sgpr_workgroup_id_y 0
		.amdhsa_system_sgpr_workgroup_id_z 0
		.amdhsa_system_sgpr_workgroup_info 0
		.amdhsa_system_vgpr_workitem_id 0
		.amdhsa_next_free_vgpr 256
		.amdhsa_next_free_sgpr 102
		.amdhsa_accum_offset 256
		.amdhsa_reserve_vcc 1
		.amdhsa_float_round_mode_32 0
		.amdhsa_float_round_mode_16_64 0
		.amdhsa_float_denorm_mode_32 3
		.amdhsa_float_denorm_mode_16_64 3
		.amdhsa_dx10_clamp 1
		.amdhsa_ieee_mode 1
		.amdhsa_fp16_overflow 0
		.amdhsa_tg_split 0
		.amdhsa_exception_fp_ieee_invalid_op 0
		.amdhsa_exception_fp_denorm_src 0
		.amdhsa_exception_fp_ieee_div_zero 0
		.amdhsa_exception_fp_ieee_overflow 0
		.amdhsa_exception_fp_ieee_underflow 0
		.amdhsa_exception_fp_ieee_inexact 0
		.amdhsa_exception_int_div_zero 0
	.end_amdhsa_kernel

amdhsa.kernels:
  - .agpr_count:     0
    .args:
      - .offset:         0
        .size:           168
        .value_kind:     by_value
      - .offset:         168
        .size:           4
        .value_kind:     hidden_block_count_x
      - .offset:         172
        .size:           4
        .value_kind:     hidden_block_count_y
      - .offset:         176
        .size:           4
        .value_kind:     hidden_block_count_z
      - .offset:         180
        .size:           2
        .value_kind:     hidden_group_size_x
      - .offset:         182
        .size:           2
        .value_kind:     hidden_group_size_y
      - .offset:         184
        .size:           2
        .value_kind:     hidden_group_size_z
      - .offset:         186
        .size:           2
        .value_kind:     hidden_remainder_x
      - .offset:         188
        .size:           2
        .value_kind:     hidden_remainder_y
      - .offset:         190
        .size:           2
        .value_kind:     hidden_remainder_z
      - .offset:         208
        .size:           8
        .value_kind:     hidden_global_offset_x
      - .offset:         216
        .size:           8
        .value_kind:     hidden_global_offset_y
      - .offset:         224
        .size:           8
        .value_kind:     hidden_global_offset_z
      - .offset:         232
        .size:           2
        .value_kind:     hidden_grid_dims
      - .offset:         288
        .size:           4
        .value_kind:     hidden_dynamic_lds_size
    .group_segment_fixed_size: 0
    .kernarg_segment_align: 8
    .kernarg_segment_size: 424
    .language:       OpenCL C
    .language_version:
      - 2
      - 0
    .max_flat_workgroup_size: 512
    .name:           _Z6mk_fwd4Args
    .private_segment_fixed_size: 0
    .sgpr_count:     108
    .sgpr_spill_count: 235
    .symbol:         _Z6mk_fwd4Args.kd
    .uniform_work_group_size: 1
    .uses_dynamic_stack: false
    .vgpr_count:     256
    .vgpr_spill_count: 0
    .wavefront_size: 64
